# gate GEMM merge epilogue: Y-tile loads of row-group batches 2-4 issued up to one batch early into spare VGPRs, vmcnt waits recomputed per branch path (simulated); on top of SEL optimisations
# speedup vs baseline: 1.0239x; 1.0013x over previous
; __device__ __forceinline__ unsigned pk2h(float lo, float hi) { f32x2 v = {lo, hi}; f16x2 h = __builtin_convertvector(v, f16x2); return __builtin_bit_cast(unsigned, h); }
;     __device__ __forceinline__ void operator()(const f32x4 (&acc)[2][2][4][2], const Unit& u, int wr, int wc, int fr, int fq) const {
;     ...
;                 for (int bj = 0; bj < 2; ++bj) yv[m][bj] = *(const g_f16x8*)(Yb + offa + (size_t)m * 16 * 1024 + bj * HALF);
;     ...
;                     f32x4 a0 = acc[ai][bj][m][0], a1 = acc[ai][bj][m][1];
;                     if constexpr (I8) { const i32x4 i0 = __builtin_bit_cast(i32x4, a0), i1 = __builtin_bit_cast(i32x4, a1);
;                         a0 = (f32x4){(float)i0.x, (float)i0.y, (float)i0.z, (float)i0.w} * sv[bj][0]; a1 = (f32x4){(float)i1.x, (float)i1.y, (float)i1.z, (float)i1.w} * sv[bj][1]; }
;                     const f32x4 g0 = a0 * rs[ai][m] + bv[bj][0], g1 = a1 * rs[ai][m] + bv[bj][1];
;                     const f16x8 yy = yv[m][bj];
;                     float z[8];
; #pragma unroll
;                     for (int e = 0; e < 4; ++e) { z[e] = (float)yy[e] * __builtin_amdgcn_rcpf(1.f + __builtin_amdgcn_exp2f(-LOG2E * g0[e])); z[4 + e] = (float)yy[4 + e] * __builtin_amdgcn_rcpf(1.f + __builtin_amdgcn_exp2f(-LOG2E * g1[e])); }
;                     if (br == 2) {
; #pragma unroll
;                         for (int e = 0; e < 8; ++e) z[e] += (float)za[bj][e] + (float)zb[bj][e]; }
;                     u32x4 w; w.x = pk2h(z[0], z[1]); w.y = pk2h(z[2], z[3]); w.z = pk2h(z[4], z[5]); w.w = pk2h(z[6], z[7]);
;                     f16* dst = (br == 2) ? merged : Yb;
;                     gst16(dst + off + bj * HALF, w); } } } }
.LBB0_1234:
	v_cvt_pk_f16_f32 v192, v180, v181
	v_cvt_f32_i32_e32 v180, v172
	v_cvt_f32_i32_e32 v172, v166
	v_cvt_pk_f16_f32 v191, v182, v183
	v_cvt_f32_i32_e32 v182, v167
	v_cvt_f32_i32_e32 v170, v170
	s_waitcnt lgkmcnt(0)
	v_mul_f32_e32 v167, v30, v172
	v_fma_f32 v167, v226, v167, v26
	v_mul_f32_e32 v167, 0xbfb8aa3b, v167
	v_exp_f32_e32 v167, v167
	v_cvt_f32_i32_e32 v171, v171
	v_mul_f32_e32 v166, v38, v170
	v_fma_f32 v166, v226, v166, v34
	v_add_f32_e32 v167, 1.0, v167
	v_rcp_f32_e32 v170, v167
	v_mul_f32_e32 v167, v39, v171
	v_fma_f32 v167, v226, v167, v35
	v_mul_f32_e32 v166, 0xbfb8aa3b, v166
	v_mul_f32_e32 v167, 0xbfb8aa3b, v167
	v_exp_f32_e32 v166, v166
	v_exp_f32_e32 v167, v167
	v_mul_f32_e32 v171, v31, v182
	v_fma_f32 v171, v226, v171, v27
	v_mul_f32_e32 v171, 0xbfb8aa3b, v171
	v_add_f32_e32 v166, 1.0, v166
	v_add_f32_e32 v167, 1.0, v167
	v_exp_f32_e32 v171, v171
	v_cvt_f32_i32_e32 v181, v173
	v_rcp_f32_e32 v166, v166
	v_rcp_f32_e32 v167, v167
	s_waitcnt vmcnt(2)
	v_cvt_f32_f16_sdwa v173, v186 dst_sel:DWORD dst_unused:UNUSED_PAD src0_sel:WORD_1
	v_cvt_f32_f16_e32 v172, v186
	v_add_f32_e32 v171, 1.0, v171
	v_rcp_f32_e32 v171, v171
	v_cvt_pk_f16_f32 v190, v178, v179
	v_pk_mul_f32 v[166:167], v[166:167], v[172:173]
	v_cvt_f32_f16_sdwa v173, v188 dst_sel:DWORD dst_unused:UNUSED_PAD src0_sel:WORD_1
	v_cvt_f32_f16_e32 v172, v188
	v_cvt_pk_f16_f32 v193, v184, v185
	v_lshl_add_u64 v[178:179], v[228:229], 1, s[46:47]
	s_mov_b64 s[52:53], -1
	v_pk_mul_f32 v[170:171], v[170:171], v[172:173]
	v_mul_f32_e32 v172, v40, v180
	v_mul_f32_e32 v173, v41, v181
	v_fma_f32 v172, v226, v172, v36
	v_fma_f32 v173, v226, v173, v37
	v_mul_f32_e32 v172, 0xbfb8aa3b, v172
	v_mul_f32_e32 v173, 0xbfb8aa3b, v173
	v_exp_f32_e32 v172, v172
	v_exp_f32_e32 v173, v173
	v_cvt_f32_f16_sdwa v181, v187 dst_sel:DWORD dst_unused:UNUSED_PAD src0_sel:WORD_1
	v_cvt_f32_f16_e32 v180, v187
	v_add_f32_e32 v172, 1.0, v172
	v_add_f32_e32 v173, 1.0, v173
	v_rcp_f32_e32 v172, v172
	v_rcp_f32_e32 v173, v173
	s_andn2_b64 vcc, exec, s[50:51]
	global_store_dwordx4 v[178:179], v[190:193], off
	v_lshl_add_u64 v[222:223], v[228:229], 1, s[48:49]
	s_mov_b64 s[28:29], 0x10000
	v_lshl_add_u64 v[222:223], v[222:223], 0, s[28:29]
	global_load_dwordx4 v[238:241], v[222:223], off
	global_load_dwordx4 v[246:249], v[222:223], off offset:256
	v_pk_mul_f32 v[172:173], v[172:173], v[180:181]
	v_cndmask_b32_e64 v180, 0, 1, s[50:51]
	v_cmp_ne_u32_e64 s[38:39], 1, v180
	s_cbranch_vccnz .LBB0_1236
	s_mov_b64 s[52:53], 0
.LBB0_1236:
	v_cvt_f32_i32_e32 v168, v168
	v_cvt_f32_i32_e32 v169, v169
	v_cvt_f32_f16_sdwa v181, v189 dst_sel:DWORD dst_unused:UNUSED_PAD src0_sel:WORD_1
	v_cvt_f32_f16_e32 v180, v189
	v_mul_f32_e32 v168, v32, v168
	v_mul_f32_e32 v169, v33, v169
	v_fma_f32 v168, v226, v168, v28
	v_fma_f32 v169, v226, v169, v29
	v_mul_f32_e32 v168, 0xbfb8aa3b, v168
	v_mul_f32_e32 v169, 0xbfb8aa3b, v169
	v_exp_f32_e32 v168, v168
	v_exp_f32_e32 v169, v169
	s_andn2_b64 vcc, exec, s[52:53]
	v_add_f32_e32 v168, 1.0, v168
	v_add_f32_e32 v169, 1.0, v169
	v_rcp_f32_e32 v168, v168
	v_rcp_f32_e32 v169, v169
	s_nop 0
	v_pk_mul_f32 v[168:169], v[168:169], v[180:181]
	s_cbranch_vccnz .LBB0_1238
	v_cvt_f32_f16_sdwa v181, v42 dst_sel:DWORD dst_unused:UNUSED_PAD src0_sel:WORD_1
	v_cvt_f32_f16_e32 v180, v42
	s_waitcnt vmcnt(3)
	v_cvt_f32_f16_sdwa v183, v46 dst_sel:DWORD dst_unused:UNUSED_PAD src0_sel:WORD_1
	v_cvt_f32_f16_e32 v182, v46
	v_cvt_f32_f16_sdwa v185, v43 dst_sel:DWORD dst_unused:UNUSED_PAD src0_sel:WORD_1
	v_cvt_f32_f16_e32 v184, v43
	v_cvt_f32_f16_sdwa v187, v47 dst_sel:DWORD dst_unused:UNUSED_PAD src0_sel:WORD_1
	v_cvt_f32_f16_e32 v186, v47
	v_cvt_f32_f16_sdwa v189, v44 dst_sel:DWORD dst_unused:UNUSED_PAD src0_sel:WORD_1
	v_cvt_f32_f16_e32 v188, v44
	v_cvt_f32_f16_sdwa v191, v48 dst_sel:DWORD dst_unused:UNUSED_PAD src0_sel:WORD_1
	v_cvt_f32_f16_e32 v190, v48
	v_cvt_f32_f16_sdwa v193, v45 dst_sel:DWORD dst_unused:UNUSED_PAD src0_sel:WORD_1
	v_cvt_f32_f16_e32 v192, v45
	v_cvt_f32_f16_sdwa v231, v49 dst_sel:DWORD dst_unused:UNUSED_PAD src0_sel:WORD_1
	v_cvt_f32_f16_e32 v230, v49
	v_pk_add_f32 v[180:181], v[182:183], v[180:181]
	v_pk_add_f32 v[182:183], v[186:187], v[184:185]
	v_pk_add_f32 v[184:185], v[190:191], v[188:189]
	v_pk_add_f32 v[186:187], v[230:231], v[192:193]
	v_pk_add_f32 v[166:167], v[166:167], v[180:181]
	v_pk_add_f32 v[172:173], v[172:173], v[182:183]
	v_pk_add_f32 v[170:171], v[170:171], v[184:185]
	v_pk_add_f32 v[168:169], v[168:169], v[186:187]
	v_bfrev_b32_e32 v230, 1
	s_branch .LBB0_1239

; __device__ __forceinline__ unsigned pk2h(float lo, float hi) { f32x2 v = {lo, hi}; f16x2 h = __builtin_convertvector(v, f16x2); return __builtin_bit_cast(unsigned, h); }
;     __device__ __forceinline__ void operator()(const f32x4 (&acc)[2][2][4][2], const Unit& u, int wr, int wc, int fr, int fq) const {
;     ...
;                 for (int bj = 0; bj < 2; ++bj) yv[m][bj] = *(const g_f16x8*)(Yb + offa + (size_t)m * 16 * 1024 + bj * HALF);
; #pragma unroll
;             for (int m = 2 * mp; m < 2 * mp + 2; ++m) { const size_t off = offa + (size_t)m * 16 * 1024;
;                 f16x8 za[2], zb[2];
;                 if (br == 2) {
; #pragma unroll
;                     for (int bj = 0; bj < 2; ++bj) { za[bj] = *(const g_f16x8*)(Y + off + bj * HALF); zb[bj] = *(const g_f16x8*)(Y + YSTR + off + bj * HALF); } }
; #pragma unroll
;                 for (int bj = 0; bj < 2; ++bj) {
;                     f32x4 a0 = acc[ai][bj][m][0], a1 = acc[ai][bj][m][1];
;                     if constexpr (I8) { const i32x4 i0 = __builtin_bit_cast(i32x4, a0), i1 = __builtin_bit_cast(i32x4, a1);
;                         a0 = (f32x4){(float)i0.x, (float)i0.y, (float)i0.z, (float)i0.w} * sv[bj][0]; a1 = (f32x4){(float)i1.x, (float)i1.y, (float)i1.z, (float)i1.w} * sv[bj][1]; }
;                     const f32x4 g0 = a0 * rs[ai][m] + bv[bj][0], g1 = a1 * rs[ai][m] + bv[bj][1];
;                     const f16x8 yy = yv[m][bj];
;                     float z[8];
; #pragma unroll
;                     for (int e = 0; e < 4; ++e) { z[e] = (float)yy[e] * __builtin_amdgcn_rcpf(1.f + __builtin_amdgcn_exp2f(-LOG2E * g0[e])); z[4 + e] = (float)yy[4 + e] * __builtin_amdgcn_rcpf(1.f + __builtin_amdgcn_exp2f(-LOG2E * g1[e])); }
;                     if (br == 2) {
; #pragma unroll
;                         for (int e = 0; e < 8; ++e) z[e] += (float)za[bj][e] + (float)zb[bj][e]; }
;                     u32x4 w; w.x = pk2h(z[0], z[1]); w.y = pk2h(z[2], z[3]); w.z = pk2h(z[4], z[5]); w.w = pk2h(z[6], z[7]);
;                     f16* dst = (br == 2) ? merged : Yb;
;                     gst16(dst + off + bj * HALF, w); } } } }
.LBB0_1239:
	v_cvt_pk_f16_f32 v180, v166, v167
	v_cvt_pk_f16_f32 v181, v172, v173
	v_cvt_pk_f16_f32 v182, v170, v171
	v_cvt_pk_f16_f32 v183, v168, v169
	s_and_b64 vcc, exec, s[36:37]
	global_store_dwordx4 v[178:179], v[180:183], off offset:256
	s_cbranch_vccnz .LBB0_1241
	v_mov_b64_e32 v[42:43], 0x8000
	v_lshl_add_u64 v[42:43], v[228:229], 1, v[42:43]
	v_lshl_add_u64 v[44:45], s[40:41], 0, v[42:43]
	s_waitcnt vmcnt(4)
	v_lshl_add_u64 v[46:47], s[44:45], 0, v[42:43]
	global_load_dwordx4 v[58:61], v[44:45], off
	s_nop 0
	global_load_dwordx4 v[42:45], v[44:45], off offset:256
	s_nop 0
	global_load_dwordx4 v[66:69], v[46:47], off
	s_nop 0
	global_load_dwordx4 v[46:49], v[46:47], off offset:256
.LBB0_1241:
	v_cvt_f32_i32_e32 v166, v154
	v_cvt_f32_i32_e32 v167, v155
	v_cvt_f32_i32_e32 v158, v158
	v_cvt_f32_i32_e32 v159, v159
	v_mul_f32_e32 v155, v54, v166
	v_fma_f32 v155, v227, v155, v50
	v_mul_f32_e32 v155, 0xbfb8aa3b, v155
	v_exp_f32_e32 v155, v155
	v_cvt_f32_i32_e32 v168, v156
	v_mul_f32_e32 v154, v70, v158
	v_fma_f32 v154, v227, v154, v62
	v_add_f32_e32 v155, 1.0, v155
	v_rcp_f32_e32 v156, v155
	v_mul_f32_e32 v155, v71, v159
	v_fma_f32 v155, v227, v155, v63
	v_mul_f32_e32 v154, 0xbfb8aa3b, v154
	v_mul_f32_e32 v155, 0xbfb8aa3b, v155
	v_exp_f32_e32 v154, v154
	v_exp_f32_e32 v155, v155
	v_cvt_f32_i32_e32 v169, v157
	v_mul_f32_e32 v157, v55, v167
	v_fma_f32 v157, v227, v157, v51
	v_mul_f32_e32 v157, 0xbfb8aa3b, v157
	v_add_f32_e32 v154, 1.0, v154
	v_add_f32_e32 v155, 1.0, v155
	v_exp_f32_e32 v157, v157
	v_rcp_f32_e32 v154, v154
	v_rcp_f32_e32 v155, v155
	s_cmp_lg_u64 s[36:37], 0
	s_cbranch_scc0 .Lg3w_30558
	s_waitcnt vmcnt(5)
	s_branch .Lg3j_30558
.Lg3w_30558:
	s_waitcnt vmcnt(3)
.Lg3j_30558:
	v_cvt_f32_f16_sdwa v159, v174 dst_sel:DWORD dst_unused:UNUSED_PAD src0_sel:WORD_1
	v_cvt_f32_f16_e32 v158, v174
	v_add_f32_e32 v157, 1.0, v157
	v_rcp_f32_e32 v157, v157
	v_cvt_f32_i32_e32 v160, v160
	v_pk_mul_f32 v[154:155], v[154:155], v[158:159]
	v_cvt_f32_f16_sdwa v159, v176 dst_sel:DWORD dst_unused:UNUSED_PAD src0_sel:WORD_1
	v_cvt_f32_f16_e32 v158, v176
	v_cvt_f32_i32_e32 v161, v161
	v_cvt_f32_f16_sdwa v167, v175 dst_sel:DWORD dst_unused:UNUSED_PAD src0_sel:WORD_1
	v_cvt_f32_f16_e32 v166, v175
	v_pk_mul_f32 v[156:157], v[156:157], v[158:159]
	v_mul_f32_e32 v159, v56, v168
	v_fma_f32 v159, v227, v159, v52
	v_mul_f32_e32 v159, 0xbfb8aa3b, v159
	v_exp_f32_e32 v159, v159
	v_mul_f32_e32 v158, v72, v160
	v_fma_f32 v158, v227, v158, v64
	v_mul_f32_e32 v158, 0xbfb8aa3b, v158
	v_add_f32_e32 v159, 1.0, v159
	v_rcp_f32_e32 v160, v159
	v_mul_f32_e32 v159, v73, v161
	v_fma_f32 v159, v227, v159, v65
	v_mul_f32_e32 v159, 0xbfb8aa3b, v159
	v_exp_f32_e32 v158, v158
	v_exp_f32_e32 v159, v159
	v_mul_f32_e32 v161, v57, v169
	v_fma_f32 v161, v227, v161, v53
	v_mul_f32_e32 v161, 0xbfb8aa3b, v161
	v_add_f32_e32 v158, 1.0, v158
	v_add_f32_e32 v159, 1.0, v159
	v_exp_f32_e32 v161, v161
	v_rcp_f32_e32 v158, v158
	v_rcp_f32_e32 v159, v159
	s_and_b64 vcc, exec, s[36:37]
	v_add_f32_e32 v161, 1.0, v161
	v_rcp_f32_e32 v161, v161
	v_pk_mul_f32 v[158:159], v[158:159], v[166:167]
	v_cvt_f32_f16_sdwa v167, v177 dst_sel:DWORD dst_unused:UNUSED_PAD src0_sel:WORD_1
	v_cvt_f32_f16_e32 v166, v177
	v_pk_mul_f32 v[160:161], v[160:161], v[166:167]
	s_cbranch_vccnz .LBB0_1243
	v_cvt_f32_f16_sdwa v167, v58 dst_sel:DWORD dst_unused:UNUSED_PAD src0_sel:WORD_1
	v_cvt_f32_f16_e32 v166, v58
	s_waitcnt vmcnt(1)
	v_cvt_f32_f16_sdwa v169, v66 dst_sel:DWORD dst_unused:UNUSED_PAD src0_sel:WORD_1
	v_cvt_f32_f16_e32 v168, v66
	v_cvt_f32_f16_sdwa v171, v59 dst_sel:DWORD dst_unused:UNUSED_PAD src0_sel:WORD_1
	v_cvt_f32_f16_e32 v170, v59
	v_cvt_f32_f16_sdwa v173, v67 dst_sel:DWORD dst_unused:UNUSED_PAD src0_sel:WORD_1
	v_cvt_f32_f16_e32 v172, v67
	v_cvt_f32_f16_sdwa v175, v60 dst_sel:DWORD dst_unused:UNUSED_PAD src0_sel:WORD_1
	v_cvt_f32_f16_e32 v174, v60
	v_cvt_f32_f16_sdwa v177, v68 dst_sel:DWORD dst_unused:UNUSED_PAD src0_sel:WORD_1
	v_cvt_f32_f16_e32 v176, v68
	v_cvt_f32_f16_sdwa v181, v61 dst_sel:DWORD dst_unused:UNUSED_PAD src0_sel:WORD_1
	v_cvt_f32_f16_e32 v180, v61
	v_cvt_f32_f16_sdwa v183, v69 dst_sel:DWORD dst_unused:UNUSED_PAD src0_sel:WORD_1
	v_cvt_f32_f16_e32 v182, v69
	v_pk_add_f32 v[166:167], v[168:169], v[166:167]
	v_pk_add_f32 v[168:169], v[172:173], v[170:171]
	v_pk_add_f32 v[170:171], v[176:177], v[174:175]
	v_pk_add_f32 v[172:173], v[182:183], v[180:181]
	v_pk_add_f32 v[154:155], v[154:155], v[166:167]
	v_pk_add_f32 v[158:159], v[158:159], v[168:169]
	v_pk_add_f32 v[156:157], v[156:157], v[170:171]
	v_pk_add_f32 v[160:161], v[160:161], v[172:173]
.LBB0_1243:
	s_mov_b32 s26, 0x8000
	v_cvt_pk_f16_f32 v154, v154, v155
	v_cvt_pk_f16_f32 v155, v158, v159
	v_add_co_u32_e32 v158, vcc, s26, v178
	v_cvt_pk_f16_f32 v156, v156, v157
	v_cvt_pk_f16_f32 v157, v160, v161
	v_addc_co_u32_e32 v159, vcc, 0, v179, vcc
	global_store_dwordx4 v[158:159], v[154:157], off
	v_cvt_f32_i32_e32 v150, v150
	v_cvt_f32_i32_e32 v151, v151
	v_cvt_f32_i32_e32 v154, v152
	v_cvt_f32_i32_e32 v152, v146
	v_cvt_f32_i32_e32 v156, v147
	v_mul_f32_e32 v146, v38, v150
	v_fma_f32 v146, v227, v146, v34
	v_mul_f32_e32 v147, v30, v152
	v_fma_f32 v147, v227, v147, v26
	v_mul_f32_e32 v147, 0xbfb8aa3b, v147
	v_exp_f32_e32 v147, v147
	v_mul_f32_e32 v146, 0xbfb8aa3b, v146
	v_exp_f32_e32 v146, v146
	v_cvt_f32_i32_e32 v155, v153
	v_add_f32_e32 v147, 1.0, v147
	v_rcp_f32_e32 v150, v147
	v_mul_f32_e32 v147, v39, v151
	v_fma_f32 v147, v227, v147, v35
	v_mul_f32_e32 v147, 0xbfb8aa3b, v147
	v_exp_f32_e32 v147, v147
	v_mul_f32_e32 v151, v31, v156
	v_fma_f32 v151, v227, v151, v27
	v_mul_f32_e32 v151, 0xbfb8aa3b, v151
	v_add_f32_e32 v146, 1.0, v146
	v_add_f32_e32 v147, 1.0, v147
	v_exp_f32_e32 v151, v151
	v_rcp_f32_e32 v146, v146
	v_rcp_f32_e32 v147, v147
	s_cmp_lg_u64 s[36:37], 0
	s_cbranch_scc0 .Lg3w_30664
	s_waitcnt vmcnt(5)
	s_branch .Lg3j_30664

;     __device__ __forceinline__ void operator()(const f32x4 (&acc)[2][2][4][2], const Unit& u, int wr, int wc, int fr, int fq) const {
;     ...
;                     f32x4 a0 = acc[ai][bj][m][0], a1 = acc[ai][bj][m][1];
;                     if constexpr (I8) { const i32x4 i0 = __builtin_bit_cast(i32x4, a0), i1 = __builtin_bit_cast(i32x4, a1);
;                         a0 = (f32x4){(float)i0.x, (float)i0.y, (float)i0.z, (float)i0.w} * sv[bj][0]; a1 = (f32x4){(float)i1.x, (float)i1.y, (float)i1.z, (float)i1.w} * sv[bj][1]; }
;                     const f32x4 g0 = a0 * rs[ai][m] + bv[bj][0], g1 = a1 * rs[ai][m] + bv[bj][1];
;                     const f16x8 yy = yv[m][bj];
;                     float z[8];
; #pragma unroll
;                     for (int e = 0; e < 4; ++e) { z[e] = (float)yy[e] * __builtin_amdgcn_rcpf(1.f + __builtin_amdgcn_exp2f(-LOG2E * g0[e])); z[4 + e] = (float)yy[4 + e] * __builtin_amdgcn_rcpf(1.f + __builtin_amdgcn_exp2f(-LOG2E * g1[e])); }
;                     if (br == 2) {
; #pragma unroll
;                         for (int e = 0; e < 8; ++e) z[e] += (float)za[bj][e] + (float)zb[bj][e]; }
.Lg3j_30664:
	v_cvt_f32_f16_sdwa v153, v162 dst_sel:DWORD dst_unused:UNUSED_PAD src0_sel:WORD_1
	v_cvt_f32_f16_e32 v152, v162
	v_add_f32_e32 v151, 1.0, v151
	v_rcp_f32_e32 v151, v151
	s_mov_b64 s[50:51], -1
	v_pk_mul_f32 v[146:147], v[146:147], v[152:153]
	v_cvt_f32_f16_sdwa v153, v164 dst_sel:DWORD dst_unused:UNUSED_PAD src0_sel:WORD_1
	v_cvt_f32_f16_e32 v152, v164
	s_and_b64 vcc, exec, s[38:39]
	v_pk_mul_f32 v[150:151], v[150:151], v[152:153]
	v_mul_f32_e32 v152, v40, v154
	v_mul_f32_e32 v153, v41, v155
	v_fma_f32 v152, v227, v152, v36
	v_fma_f32 v153, v227, v153, v37
	v_mul_f32_e32 v152, 0xbfb8aa3b, v152
	v_mul_f32_e32 v153, 0xbfb8aa3b, v153
	v_exp_f32_e32 v152, v152
	v_exp_f32_e32 v153, v153
	v_cvt_f32_f16_sdwa v155, v163 dst_sel:DWORD dst_unused:UNUSED_PAD src0_sel:WORD_1
	v_cvt_f32_f16_e32 v154, v163
	v_add_f32_e32 v152, 1.0, v152
	v_add_f32_e32 v153, 1.0, v153
	v_rcp_f32_e32 v152, v152
	v_rcp_f32_e32 v153, v153
	s_nop 0
	v_pk_mul_f32 v[152:153], v[152:153], v[154:155]
	s_cbranch_vccnz .LBB0_1245
	s_mov_b64 s[50:51], 0

;     __device__ __forceinline__ void operator()(const f32x4 (&acc)[2][2][4][2], const Unit& u, int wr, int wc, int fr, int fq) const {
;     ...
;             const int rowa = row0 + ai * HALF; const size_t offa = (size_t)rowa * 1024 + (size_t)(rowa >> 12) * GAPY + col0;
; #pragma unroll
;             for (int mp = 0; mp < 2; ++mp) {
;             f16x8 yv[4][2];
; #pragma unroll
;             for (int m = 2 * mp; m < 2 * mp + 2; ++m)
; #pragma unroll
;                 for (int bj = 0; bj < 2; ++bj) yv[m][bj] = *(const g_f16x8*)(Yb + offa + (size_t)m * 16 * 1024 + bj * HALF);
; #pragma unroll
;             for (int m = 2 * mp; m < 2 * mp + 2; ++m) { const size_t off = offa + (size_t)m * 16 * 1024;
;                 f16x8 za[2], zb[2];
;                 if (br == 2) {
; #pragma unroll
;                     for (int bj = 0; bj < 2; ++bj) { za[bj] = *(const g_f16x8*)(Y + off + bj * HALF); zb[bj] = *(const g_f16x8*)(Y + YSTR + off + bj * HALF); } }
.LBB0_1247:
	s_mov_b64 s[28:29], 0x8000
	v_lshl_add_u64 v[158:159], v[178:179], 0, s[28:29]
	v_cvt_pk_f16_f32 v154, v146, v147
	v_cvt_pk_f16_f32 v155, v152, v153
	v_cvt_pk_f16_f32 v156, v150, v151
	v_cvt_pk_f16_f32 v157, v148, v149
	v_add_co_u32_e32 v146, vcc, 0x10000, v224
	global_store_dwordx4 v[158:159], v[154:157], off offset:256
	s_nop 0
	v_addc_co_u32_e32 v147, vcc, 0, v225, vcc
	v_add_co_u32_e32 v146, vcc, 0x18000, v224
	s_nop 1
	v_addc_co_u32_e32 v147, vcc, 0, v225, vcc
	global_load_dwordx4 v[150:153], v[146:147], off
	s_nop 0
	global_load_dwordx4 v[146:149], v[146:147], off offset:256
	v_lshl_add_u64 v[222:223], v[228:229], 1, s[48:49]
	s_mov_b64 s[28:29], 0x40000
	v_lshl_add_u64 v[222:223], v[222:223], 0, s[28:29]
	global_load_dwordx4 v[174:177], v[222:223], off
	global_load_dwordx4 v[180:183], v[222:223], off offset:256
	s_and_b64 vcc, exec, s[36:37]
	s_cbranch_vccnz .LBB0_1249
	v_mov_b64_e32 v[42:43], 0x10000
	v_lshl_add_u64 v[42:43], v[228:229], 1, v[42:43]
	v_lshl_add_u64 v[44:45], s[40:41], 0, v[42:43]
	s_waitcnt vmcnt(6)
	v_lshl_add_u64 v[46:47], s[44:45], 0, v[42:43]
	global_load_dwordx4 v[58:61], v[44:45], off
	s_nop 0
	global_load_dwordx4 v[42:45], v[44:45], off offset:256
	s_nop 0
	global_load_dwordx4 v[66:69], v[46:47], off
	s_nop 0
	global_load_dwordx4 v[46:49], v[46:47], off offset:256
.LBB0_1249:
	v_cvt_f32_i32_e32 v162, v138
	v_cvt_f32_i32_e32 v163, v139
	v_cvt_f32_i32_e32 v142, v142
	v_cvt_f32_i32_e32 v143, v143
	v_mul_f32_e32 v139, v54, v162
	v_fma_f32 v139, v220, v139, v50
	v_mul_f32_e32 v139, 0xbfb8aa3b, v139
	v_exp_f32_e32 v139, v139
	v_cvt_f32_i32_e32 v164, v140
	v_mul_f32_e32 v138, v70, v142
	v_fma_f32 v138, v220, v138, v62
	v_add_f32_e32 v139, 1.0, v139
	v_rcp_f32_e32 v140, v139
	v_mul_f32_e32 v139, v71, v143
	v_fma_f32 v139, v220, v139, v63
	v_mul_f32_e32 v138, 0xbfb8aa3b, v138
	v_mul_f32_e32 v139, 0xbfb8aa3b, v139
	v_exp_f32_e32 v138, v138
	v_exp_f32_e32 v139, v139
	v_cvt_f32_i32_e32 v165, v141
	v_mul_f32_e32 v141, v55, v163
	v_fma_f32 v141, v220, v141, v51
	v_mul_f32_e32 v141, 0xbfb8aa3b, v141
	v_add_f32_e32 v138, 1.0, v138
	v_add_f32_e32 v139, 1.0, v139
	v_exp_f32_e32 v141, v141
	v_rcp_f32_e32 v138, v138
	v_rcp_f32_e32 v139, v139
	s_cmp_lg_u64 s[36:37], 0
	s_cbranch_scc0 .Lg3w_30804
	s_waitcnt vmcnt(8)
	s_branch .Lg3j_30804

; __device__ __forceinline__ unsigned pk2h(float lo, float hi) { f32x2 v = {lo, hi}; f16x2 h = __builtin_convertvector(v, f16x2); return __builtin_bit_cast(unsigned, h); }
;     __device__ __forceinline__ void operator()(const f32x4 (&acc)[2][2][4][2], const Unit& u, int wr, int wc, int fr, int fq) const {
;     ...
;                     f32x4 a0 = acc[ai][bj][m][0], a1 = acc[ai][bj][m][1];
;                     if constexpr (I8) { const i32x4 i0 = __builtin_bit_cast(i32x4, a0), i1 = __builtin_bit_cast(i32x4, a1);
;                         a0 = (f32x4){(float)i0.x, (float)i0.y, (float)i0.z, (float)i0.w} * sv[bj][0]; a1 = (f32x4){(float)i1.x, (float)i1.y, (float)i1.z, (float)i1.w} * sv[bj][1]; }
;                     const f32x4 g0 = a0 * rs[ai][m] + bv[bj][0], g1 = a1 * rs[ai][m] + bv[bj][1];
;                     const f16x8 yy = yv[m][bj];
;                     float z[8];
; #pragma unroll
;                     for (int e = 0; e < 4; ++e) { z[e] = (float)yy[e] * __builtin_amdgcn_rcpf(1.f + __builtin_amdgcn_exp2f(-LOG2E * g0[e])); z[4 + e] = (float)yy[4 + e] * __builtin_amdgcn_rcpf(1.f + __builtin_amdgcn_exp2f(-LOG2E * g1[e])); }
;                     if (br == 2) {
; #pragma unroll
;                         for (int e = 0; e < 8; ++e) z[e] += (float)za[bj][e] + (float)zb[bj][e]; }
;                     u32x4 w; w.x = pk2h(z[0], z[1]); w.y = pk2h(z[2], z[3]); w.z = pk2h(z[4], z[5]); w.w = pk2h(z[6], z[7]);
;                     f16* dst = (br == 2) ? merged : Yb;
;                     gst16(dst + off + bj * HALF, w); } } } }
.Lg3j_30804:
	v_cvt_f32_f16_sdwa v143, v238 dst_sel:DWORD dst_unused:UNUSED_PAD src0_sel:WORD_1
	v_cvt_f32_f16_e32 v142, v238
	v_add_f32_e32 v141, 1.0, v141
	v_rcp_f32_e32 v141, v141
	v_cvt_f32_i32_e32 v144, v144
	v_pk_mul_f32 v[138:139], v[138:139], v[142:143]
	v_cvt_f32_f16_sdwa v143, v240 dst_sel:DWORD dst_unused:UNUSED_PAD src0_sel:WORD_1
	v_cvt_f32_f16_e32 v142, v240
	v_cvt_f32_i32_e32 v145, v145
	v_cvt_f32_f16_sdwa v163, v239 dst_sel:DWORD dst_unused:UNUSED_PAD src0_sel:WORD_1
	v_cvt_f32_f16_e32 v162, v239
	v_pk_mul_f32 v[140:141], v[140:141], v[142:143]
	v_mul_f32_e32 v143, v56, v164
	v_fma_f32 v143, v220, v143, v52
	v_mul_f32_e32 v143, 0xbfb8aa3b, v143
	v_exp_f32_e32 v143, v143
	v_mul_f32_e32 v142, v72, v144
	v_fma_f32 v142, v220, v142, v64
	v_mul_f32_e32 v142, 0xbfb8aa3b, v142
	v_add_f32_e32 v143, 1.0, v143
	v_rcp_f32_e32 v144, v143
	v_mul_f32_e32 v143, v73, v145
	v_mul_f32_e32 v145, v57, v165
	v_fma_f32 v143, v220, v143, v65
	v_fma_f32 v145, v220, v145, v53
	v_mul_f32_e32 v143, 0xbfb8aa3b, v143
	v_mul_f32_e32 v145, 0xbfb8aa3b, v145
	v_exp_f32_e32 v142, v142
	v_exp_f32_e32 v143, v143
	v_exp_f32_e32 v145, v145
	v_cvt_f32_f16_sdwa v159, v241 dst_sel:DWORD dst_unused:UNUSED_PAD src0_sel:WORD_1
	v_add_f32_e32 v142, 1.0, v142
	v_add_f32_e32 v143, 1.0, v143
	v_add_f32_e32 v145, 1.0, v145
	v_rcp_f32_e32 v142, v142
	v_rcp_f32_e32 v143, v143
	v_rcp_f32_e32 v145, v145
	v_cvt_f32_f16_e32 v158, v241
	s_and_b64 vcc, exec, s[36:37]
	v_pk_mul_f32 v[142:143], v[142:143], v[162:163]
	v_pk_mul_f32 v[144:145], v[144:145], v[158:159]
	s_cbranch_vccnz .LBB0_1251
	v_cvt_f32_f16_sdwa v159, v58 dst_sel:DWORD dst_unused:UNUSED_PAD src0_sel:WORD_1
	v_cvt_f32_f16_e32 v158, v58
	s_waitcnt vmcnt(1)
	v_cvt_f32_f16_sdwa v161, v66 dst_sel:DWORD dst_unused:UNUSED_PAD src0_sel:WORD_1
	v_cvt_f32_f16_e32 v160, v66
	v_cvt_f32_f16_sdwa v163, v59 dst_sel:DWORD dst_unused:UNUSED_PAD src0_sel:WORD_1
	v_cvt_f32_f16_e32 v162, v59
	v_cvt_f32_f16_sdwa v165, v67 dst_sel:DWORD dst_unused:UNUSED_PAD src0_sel:WORD_1
	v_cvt_f32_f16_e32 v164, v67
	v_cvt_f32_f16_sdwa v167, v60 dst_sel:DWORD dst_unused:UNUSED_PAD src0_sel:WORD_1
	v_cvt_f32_f16_e32 v166, v60
	v_cvt_f32_f16_sdwa v169, v68 dst_sel:DWORD dst_unused:UNUSED_PAD src0_sel:WORD_1
	v_cvt_f32_f16_e32 v168, v68
	v_cvt_f32_f16_sdwa v171, v61 dst_sel:DWORD dst_unused:UNUSED_PAD src0_sel:WORD_1
	v_cvt_f32_f16_e32 v170, v61
	v_cvt_f32_f16_sdwa v173, v69 dst_sel:DWORD dst_unused:UNUSED_PAD src0_sel:WORD_1
	v_cvt_f32_f16_e32 v172, v69
	v_pk_add_f32 v[158:159], v[160:161], v[158:159]
	v_pk_add_f32 v[160:161], v[164:165], v[162:163]
	v_pk_add_f32 v[162:163], v[168:169], v[166:167]
	v_pk_add_f32 v[164:165], v[172:173], v[170:171]
	v_pk_add_f32 v[138:139], v[138:139], v[158:159]
	v_pk_add_f32 v[142:143], v[142:143], v[160:161]
	v_pk_add_f32 v[140:141], v[140:141], v[162:163]
	v_pk_add_f32 v[144:145], v[144:145], v[164:165]
.LBB0_1251:
	s_mov_b32 s26, 0x10000
	v_cvt_pk_f16_f32 v138, v138, v139
	v_cvt_pk_f16_f32 v139, v142, v143
	v_add_co_u32_e32 v142, vcc, s26, v178
	v_cvt_pk_f16_f32 v140, v140, v141
	v_cvt_pk_f16_f32 v141, v144, v145
	v_addc_co_u32_e32 v143, vcc, 0, v179, vcc
	global_store_dwordx4 v[142:143], v[138:141], off
	v_cvt_f32_i32_e32 v134, v134
	v_cvt_f32_i32_e32 v135, v135
	v_cvt_f32_i32_e32 v138, v136
	v_cvt_f32_i32_e32 v136, v130
	v_cvt_f32_i32_e32 v140, v131
	v_mul_f32_e32 v130, v38, v134
	v_fma_f32 v130, v220, v130, v34
	v_mul_f32_e32 v131, v30, v136
	v_fma_f32 v131, v220, v131, v26
	v_mul_f32_e32 v131, 0xbfb8aa3b, v131
	v_exp_f32_e32 v131, v131
	v_mul_f32_e32 v130, 0xbfb8aa3b, v130
	v_exp_f32_e32 v130, v130
	v_cvt_f32_i32_e32 v139, v137
	v_add_f32_e32 v131, 1.0, v131
	v_rcp_f32_e32 v134, v131
	v_mul_f32_e32 v131, v39, v135
	v_fma_f32 v131, v220, v131, v35
	v_mul_f32_e32 v131, 0xbfb8aa3b, v131
	v_exp_f32_e32 v131, v131
	v_mul_f32_e32 v135, v31, v140
	v_fma_f32 v135, v220, v135, v27
	v_mul_f32_e32 v135, 0xbfb8aa3b, v135
	v_add_f32_e32 v130, 1.0, v130
	v_add_f32_e32 v131, 1.0, v131
	v_exp_f32_e32 v135, v135
	v_rcp_f32_e32 v130, v130
	v_rcp_f32_e32 v131, v131
	s_cmp_lg_u64 s[36:37], 0
	s_cbranch_scc0 .Lg3w_30910
	s_waitcnt vmcnt(8)
	s_branch .Lg3j_30910

; __device__ __forceinline__ unsigned pk2h(float lo, float hi) { f32x2 v = {lo, hi}; f16x2 h = __builtin_convertvector(v, f16x2); return __builtin_bit_cast(unsigned, h); }
;     __device__ __forceinline__ void operator()(const f32x4 (&acc)[2][2][4][2], const Unit& u, int wr, int wc, int fr, int fq) const {
;     ...
;                 for (int bj = 0; bj < 2; ++bj) yv[m][bj] = *(const g_f16x8*)(Yb + offa + (size_t)m * 16 * 1024 + bj * HALF);
; #pragma unroll
;             for (int m = 2 * mp; m < 2 * mp + 2; ++m) { const size_t off = offa + (size_t)m * 16 * 1024;
;                 f16x8 za[2], zb[2];
;                 if (br == 2) {
; #pragma unroll
;                     for (int bj = 0; bj < 2; ++bj) { za[bj] = *(const g_f16x8*)(Y + off + bj * HALF); zb[bj] = *(const g_f16x8*)(Y + YSTR + off + bj * HALF); } }
; #pragma unroll
;                 for (int bj = 0; bj < 2; ++bj) {
;                     f32x4 a0 = acc[ai][bj][m][0], a1 = acc[ai][bj][m][1];
;                     if constexpr (I8) { const i32x4 i0 = __builtin_bit_cast(i32x4, a0), i1 = __builtin_bit_cast(i32x4, a1);
;                         a0 = (f32x4){(float)i0.x, (float)i0.y, (float)i0.z, (float)i0.w} * sv[bj][0]; a1 = (f32x4){(float)i1.x, (float)i1.y, (float)i1.z, (float)i1.w} * sv[bj][1]; }
;                     const f32x4 g0 = a0 * rs[ai][m] + bv[bj][0], g1 = a1 * rs[ai][m] + bv[bj][1];
;                     const f16x8 yy = yv[m][bj];
;                     float z[8];
; #pragma unroll
;                     for (int e = 0; e < 4; ++e) { z[e] = (float)yy[e] * __builtin_amdgcn_rcpf(1.f + __builtin_amdgcn_exp2f(-LOG2E * g0[e])); z[4 + e] = (float)yy[4 + e] * __builtin_amdgcn_rcpf(1.f + __builtin_amdgcn_exp2f(-LOG2E * g1[e])); }
;                     if (br == 2) {
; #pragma unroll
;                         for (int e = 0; e < 8; ++e) z[e] += (float)za[bj][e] + (float)zb[bj][e]; }
;                     u32x4 w; w.x = pk2h(z[0], z[1]); w.y = pk2h(z[2], z[3]); w.z = pk2h(z[4], z[5]); w.w = pk2h(z[6], z[7]);
;                     f16* dst = (br == 2) ? merged : Yb;
;                     gst16(dst + off + bj * HALF, w); } } } }
.Lg3j_30910:
	v_cvt_f32_f16_sdwa v137, v246 dst_sel:DWORD dst_unused:UNUSED_PAD src0_sel:WORD_1
	v_cvt_f32_f16_e32 v136, v246
	v_add_f32_e32 v135, 1.0, v135
	v_rcp_f32_e32 v135, v135
	s_mov_b64 s[50:51], -1
	v_pk_mul_f32 v[130:131], v[130:131], v[136:137]
	v_cvt_f32_f16_sdwa v137, v248 dst_sel:DWORD dst_unused:UNUSED_PAD src0_sel:WORD_1
	v_cvt_f32_f16_e32 v136, v248
	s_and_b64 vcc, exec, s[38:39]
	v_pk_mul_f32 v[134:135], v[134:135], v[136:137]
	v_mul_f32_e32 v136, v40, v138
	v_mul_f32_e32 v137, v41, v139
	v_fma_f32 v136, v220, v136, v36
	v_fma_f32 v137, v220, v137, v37
	v_mul_f32_e32 v136, 0xbfb8aa3b, v136
	v_mul_f32_e32 v137, 0xbfb8aa3b, v137
	v_exp_f32_e32 v136, v136
	v_exp_f32_e32 v137, v137
	v_cvt_f32_f16_sdwa v139, v247 dst_sel:DWORD dst_unused:UNUSED_PAD src0_sel:WORD_1
	v_cvt_f32_f16_e32 v138, v247
	v_add_f32_e32 v136, 1.0, v136
	v_add_f32_e32 v137, 1.0, v137
	v_rcp_f32_e32 v136, v136
	v_rcp_f32_e32 v137, v137
	s_nop 0
	v_pk_mul_f32 v[136:137], v[136:137], v[138:139]
	s_cbranch_vccnz .LBB0_1253
	s_mov_b64 s[50:51], 0
.LBB0_1253:
	v_cvt_f32_i32_e32 v132, v132
	v_cvt_f32_i32_e32 v133, v133
	v_cvt_f32_f16_sdwa v139, v249 dst_sel:DWORD dst_unused:UNUSED_PAD src0_sel:WORD_1
	v_cvt_f32_f16_e32 v138, v249
	v_mul_f32_e32 v132, v32, v132
	v_mul_f32_e32 v133, v33, v133
	v_fma_f32 v132, v220, v132, v28
	v_fma_f32 v133, v220, v133, v29
	v_mul_f32_e32 v132, 0xbfb8aa3b, v132
	v_mul_f32_e32 v133, 0xbfb8aa3b, v133
	v_exp_f32_e32 v132, v132
	v_exp_f32_e32 v133, v133
	s_andn2_b64 vcc, exec, s[50:51]
	v_add_f32_e32 v132, 1.0, v132
	v_add_f32_e32 v133, 1.0, v133
	v_rcp_f32_e32 v132, v132
	v_rcp_f32_e32 v133, v133
	s_nop 0
	v_pk_mul_f32 v[132:133], v[132:133], v[138:139]
	s_cbranch_vccnz .LBB0_1255
	v_cvt_f32_f16_sdwa v139, v42 dst_sel:DWORD dst_unused:UNUSED_PAD src0_sel:WORD_1
	v_cvt_f32_f16_e32 v138, v42
	s_waitcnt vmcnt(1)
	v_cvt_f32_f16_sdwa v141, v46 dst_sel:DWORD dst_unused:UNUSED_PAD src0_sel:WORD_1
	v_cvt_f32_f16_e32 v140, v46
	v_cvt_f32_f16_sdwa v143, v43 dst_sel:DWORD dst_unused:UNUSED_PAD src0_sel:WORD_1
	v_cvt_f32_f16_e32 v142, v43
	v_cvt_f32_f16_sdwa v145, v47 dst_sel:DWORD dst_unused:UNUSED_PAD src0_sel:WORD_1
	v_cvt_f32_f16_e32 v144, v47
	v_cvt_f32_f16_sdwa v155, v44 dst_sel:DWORD dst_unused:UNUSED_PAD src0_sel:WORD_1
	v_cvt_f32_f16_e32 v154, v44
	v_cvt_f32_f16_sdwa v157, v48 dst_sel:DWORD dst_unused:UNUSED_PAD src0_sel:WORD_1
	v_cvt_f32_f16_e32 v156, v48
	v_cvt_f32_f16_sdwa v159, v45 dst_sel:DWORD dst_unused:UNUSED_PAD src0_sel:WORD_1
	v_cvt_f32_f16_e32 v158, v45
	v_cvt_f32_f16_sdwa v161, v49 dst_sel:DWORD dst_unused:UNUSED_PAD src0_sel:WORD_1
	v_cvt_f32_f16_e32 v160, v49
	v_pk_add_f32 v[138:139], v[140:141], v[138:139]
	v_pk_add_f32 v[140:141], v[144:145], v[142:143]
	v_pk_add_f32 v[142:143], v[156:157], v[154:155]
	v_pk_add_f32 v[144:145], v[160:161], v[158:159]
	v_pk_add_f32 v[130:131], v[130:131], v[138:139]
	v_pk_add_f32 v[136:137], v[136:137], v[140:141]
	v_pk_add_f32 v[134:135], v[134:135], v[142:143]
	v_pk_add_f32 v[132:133], v[132:133], v[144:145]
.LBB0_1255:
	s_mov_b64 s[28:29], 0x10000
	v_lshl_add_u64 v[142:143], v[178:179], 0, s[28:29]
	v_cvt_pk_f16_f32 v138, v130, v131
	v_cvt_pk_f16_f32 v139, v136, v137
	v_cvt_pk_f16_f32 v140, v134, v135
	v_cvt_pk_f16_f32 v141, v132, v133
	s_and_b64 vcc, exec, s[36:37]
	global_store_dwordx4 v[142:143], v[138:141], off offset:256
	v_lshl_add_u64 v[222:223], v[228:229], 1, s[48:49]
	s_mov_b64 s[28:29], 0x48000
	v_lshl_add_u64 v[222:223], v[222:223], 0, s[28:29]
	global_load_dwordx4 v[162:165], v[222:223], off
	global_load_dwordx4 v[166:169], v[222:223], off offset:256
	s_cbranch_vccnz .LBB0_1257
	v_mov_b64_e32 v[42:43], 0x18000
	v_lshl_add_u64 v[42:43], v[228:229], 1, v[42:43]
	v_lshl_add_u64 v[44:45], s[40:41], 0, v[42:43]
	s_waitcnt vmcnt(4)
	v_lshl_add_u64 v[46:47], s[44:45], 0, v[42:43]
	global_load_dwordx4 v[58:61], v[44:45], off
	s_nop 0
	global_load_dwordx4 v[42:45], v[44:45], off offset:256
	s_nop 0
	global_load_dwordx4 v[66:69], v[46:47], off
	s_nop 0
	global_load_dwordx4 v[46:49], v[46:47], off offset:256
.LBB0_1257:
	v_cvt_f32_i32_e32 v130, v122
	v_cvt_f32_i32_e32 v131, v123
	v_cvt_f32_i32_e32 v126, v126
	v_cvt_f32_i32_e32 v127, v127
	v_mul_f32_e32 v123, v54, v130
	v_fma_f32 v123, v221, v123, v50
	v_mul_f32_e32 v123, 0xbfb8aa3b, v123
	v_exp_f32_e32 v123, v123
	v_cvt_f32_i32_e32 v132, v124
	v_mul_f32_e32 v122, v70, v126
	v_fma_f32 v122, v221, v122, v62
	v_add_f32_e32 v123, 1.0, v123
	v_rcp_f32_e32 v124, v123
	v_mul_f32_e32 v123, v71, v127
	v_fma_f32 v123, v221, v123, v63
	v_mul_f32_e32 v122, 0xbfb8aa3b, v122
	v_mul_f32_e32 v123, 0xbfb8aa3b, v123
	v_exp_f32_e32 v122, v122
	v_exp_f32_e32 v123, v123
	v_cvt_f32_i32_e32 v133, v125
	v_mul_f32_e32 v125, v55, v131
	v_fma_f32 v125, v221, v125, v51
	v_mul_f32_e32 v125, 0xbfb8aa3b, v125
	v_add_f32_e32 v122, 1.0, v122
	v_add_f32_e32 v123, 1.0, v123
	v_exp_f32_e32 v125, v125
	v_rcp_f32_e32 v122, v122
	v_rcp_f32_e32 v123, v123
	s_cmp_lg_u64 s[36:37], 0
	s_cbranch_scc0 .Lg3w_31039
	s_waitcnt vmcnt(7)
	s_branch .Lg3j_31039

; __device__ __forceinline__ unsigned pk2h(float lo, float hi) { f32x2 v = {lo, hi}; f16x2 h = __builtin_convertvector(v, f16x2); return __builtin_bit_cast(unsigned, h); }
;     __device__ __forceinline__ void operator()(const f32x4 (&acc)[2][2][4][2], const Unit& u, int wr, int wc, int fr, int fq) const {
;     ...
;                     f32x4 a0 = acc[ai][bj][m][0], a1 = acc[ai][bj][m][1];
;                     if constexpr (I8) { const i32x4 i0 = __builtin_bit_cast(i32x4, a0), i1 = __builtin_bit_cast(i32x4, a1);
;                         a0 = (f32x4){(float)i0.x, (float)i0.y, (float)i0.z, (float)i0.w} * sv[bj][0]; a1 = (f32x4){(float)i1.x, (float)i1.y, (float)i1.z, (float)i1.w} * sv[bj][1]; }
;                     const f32x4 g0 = a0 * rs[ai][m] + bv[bj][0], g1 = a1 * rs[ai][m] + bv[bj][1];
;                     const f16x8 yy = yv[m][bj];
;                     float z[8];
; #pragma unroll
;                     for (int e = 0; e < 4; ++e) { z[e] = (float)yy[e] * __builtin_amdgcn_rcpf(1.f + __builtin_amdgcn_exp2f(-LOG2E * g0[e])); z[4 + e] = (float)yy[4 + e] * __builtin_amdgcn_rcpf(1.f + __builtin_amdgcn_exp2f(-LOG2E * g1[e])); }
;                     if (br == 2) {
; #pragma unroll
;                         for (int e = 0; e < 8; ++e) z[e] += (float)za[bj][e] + (float)zb[bj][e]; }
;                     u32x4 w; w.x = pk2h(z[0], z[1]); w.y = pk2h(z[2], z[3]); w.z = pk2h(z[4], z[5]); w.w = pk2h(z[6], z[7]);
;                     f16* dst = (br == 2) ? merged : Yb;
;                     gst16(dst + off + bj * HALF, w); } } } }
.Lg3j_31039:
	v_cvt_f32_f16_sdwa v127, v150 dst_sel:DWORD dst_unused:UNUSED_PAD src0_sel:WORD_1
	v_cvt_f32_f16_e32 v126, v150
	v_add_f32_e32 v125, 1.0, v125
	v_rcp_f32_e32 v125, v125
	v_cvt_f32_i32_e32 v128, v128
	v_pk_mul_f32 v[122:123], v[122:123], v[126:127]
	v_cvt_f32_f16_sdwa v127, v152 dst_sel:DWORD dst_unused:UNUSED_PAD src0_sel:WORD_1
	v_cvt_f32_f16_e32 v126, v152
	v_cvt_f32_i32_e32 v129, v129
	v_cvt_f32_f16_sdwa v131, v151 dst_sel:DWORD dst_unused:UNUSED_PAD src0_sel:WORD_1
	v_cvt_f32_f16_e32 v130, v151
	v_pk_mul_f32 v[124:125], v[124:125], v[126:127]
	v_mul_f32_e32 v127, v56, v132
	v_fma_f32 v127, v221, v127, v52
	v_mul_f32_e32 v127, 0xbfb8aa3b, v127
	v_exp_f32_e32 v127, v127
	v_mul_f32_e32 v126, v72, v128
	v_fma_f32 v126, v221, v126, v64
	v_mul_f32_e32 v126, 0xbfb8aa3b, v126
	v_add_f32_e32 v127, 1.0, v127
	v_rcp_f32_e32 v128, v127
	v_mul_f32_e32 v127, v73, v129
	v_fma_f32 v127, v221, v127, v65
	v_mul_f32_e32 v127, 0xbfb8aa3b, v127
	v_exp_f32_e32 v126, v126
	v_exp_f32_e32 v127, v127
	v_mul_f32_e32 v129, v57, v133
	v_fma_f32 v129, v221, v129, v53
	v_mul_f32_e32 v129, 0xbfb8aa3b, v129
	v_add_f32_e32 v126, 1.0, v126
	v_add_f32_e32 v127, 1.0, v127
	v_exp_f32_e32 v129, v129
	v_rcp_f32_e32 v126, v126
	v_rcp_f32_e32 v127, v127
	s_and_b64 vcc, exec, s[36:37]
	v_add_f32_e32 v129, 1.0, v129
	v_rcp_f32_e32 v129, v129
	v_pk_mul_f32 v[126:127], v[126:127], v[130:131]
	v_cvt_f32_f16_sdwa v131, v153 dst_sel:DWORD dst_unused:UNUSED_PAD src0_sel:WORD_1
	v_cvt_f32_f16_e32 v130, v153
	v_pk_mul_f32 v[128:129], v[128:129], v[130:131]
	s_cbranch_vccnz .LBB0_1259
	v_cvt_f32_f16_sdwa v131, v58 dst_sel:DWORD dst_unused:UNUSED_PAD src0_sel:WORD_1
	v_cvt_f32_f16_e32 v130, v58
	s_waitcnt vmcnt(1)
	v_cvt_f32_f16_sdwa v133, v66 dst_sel:DWORD dst_unused:UNUSED_PAD src0_sel:WORD_1
	v_cvt_f32_f16_e32 v132, v66
	v_cvt_f32_f16_sdwa v135, v59 dst_sel:DWORD dst_unused:UNUSED_PAD src0_sel:WORD_1
	v_cvt_f32_f16_e32 v134, v59
	v_cvt_f32_f16_sdwa v137, v67 dst_sel:DWORD dst_unused:UNUSED_PAD src0_sel:WORD_1
	v_cvt_f32_f16_e32 v136, v67
	v_cvt_f32_f16_sdwa v139, v60 dst_sel:DWORD dst_unused:UNUSED_PAD src0_sel:WORD_1
	v_cvt_f32_f16_e32 v138, v60
	v_cvt_f32_f16_sdwa v141, v68 dst_sel:DWORD dst_unused:UNUSED_PAD src0_sel:WORD_1
	v_cvt_f32_f16_e32 v140, v68
	v_cvt_f32_f16_sdwa v143, v61 dst_sel:DWORD dst_unused:UNUSED_PAD src0_sel:WORD_1
	v_cvt_f32_f16_e32 v142, v61
	v_cvt_f32_f16_sdwa v145, v69 dst_sel:DWORD dst_unused:UNUSED_PAD src0_sel:WORD_1
	v_cvt_f32_f16_e32 v144, v69
	v_pk_add_f32 v[130:131], v[132:133], v[130:131]
	v_pk_add_f32 v[132:133], v[136:137], v[134:135]
	v_pk_add_f32 v[134:135], v[140:141], v[138:139]
	v_pk_add_f32 v[136:137], v[144:145], v[142:143]
	v_pk_add_f32 v[122:123], v[122:123], v[130:131]
	v_pk_add_f32 v[126:127], v[126:127], v[132:133]
	v_pk_add_f32 v[124:125], v[124:125], v[134:135]
	v_pk_add_f32 v[128:129], v[128:129], v[136:137]
.LBB0_1259:
	s_mov_b32 s26, 0x18000
	v_cvt_pk_f16_f32 v122, v122, v123
	v_cvt_pk_f16_f32 v123, v126, v127
	v_add_co_u32_e32 v126, vcc, s26, v178
	v_cvt_pk_f16_f32 v124, v124, v125
	v_cvt_pk_f16_f32 v125, v128, v129
	v_addc_co_u32_e32 v127, vcc, 0, v179, vcc
	global_store_dwordx4 v[126:127], v[122:125], off
	v_cvt_f32_i32_e32 v118, v118
	v_cvt_f32_i32_e32 v119, v119
	v_cvt_f32_i32_e32 v122, v120
	v_cvt_f32_i32_e32 v120, v114
	v_cvt_f32_i32_e32 v124, v115
	v_mul_f32_e32 v114, v38, v118
	v_fma_f32 v114, v221, v114, v34
	v_mul_f32_e32 v115, v30, v120
	v_fma_f32 v115, v221, v115, v26
	v_mul_f32_e32 v115, 0xbfb8aa3b, v115
	v_exp_f32_e32 v115, v115
	v_mul_f32_e32 v114, 0xbfb8aa3b, v114
	v_exp_f32_e32 v114, v114
	v_cvt_f32_i32_e32 v123, v121
	v_add_f32_e32 v115, 1.0, v115
	v_rcp_f32_e32 v118, v115
	v_mul_f32_e32 v115, v39, v119
	v_fma_f32 v115, v221, v115, v35
	v_mul_f32_e32 v115, 0xbfb8aa3b, v115
	v_exp_f32_e32 v115, v115
	v_mul_f32_e32 v119, v31, v124
	v_fma_f32 v119, v221, v119, v27
	v_mul_f32_e32 v119, 0xbfb8aa3b, v119
	v_add_f32_e32 v114, 1.0, v114
	v_add_f32_e32 v115, 1.0, v115
	v_exp_f32_e32 v119, v119
	v_rcp_f32_e32 v114, v114
	v_rcp_f32_e32 v115, v115
	s_cmp_lg_u64 s[36:37], 0
	s_cbranch_scc0 .Lg3w_31145
	s_waitcnt vmcnt(7)
	s_branch .Lg3j_31145

;     __device__ __forceinline__ void operator()(const f32x4 (&acc)[2][2][4][2], const Unit& u, int wr, int wc, int fr, int fq) const {
;     ...
;                     f32x4 a0 = acc[ai][bj][m][0], a1 = acc[ai][bj][m][1];
;                     if constexpr (I8) { const i32x4 i0 = __builtin_bit_cast(i32x4, a0), i1 = __builtin_bit_cast(i32x4, a1);
;                         a0 = (f32x4){(float)i0.x, (float)i0.y, (float)i0.z, (float)i0.w} * sv[bj][0]; a1 = (f32x4){(float)i1.x, (float)i1.y, (float)i1.z, (float)i1.w} * sv[bj][1]; }
;                     const f32x4 g0 = a0 * rs[ai][m] + bv[bj][0], g1 = a1 * rs[ai][m] + bv[bj][1];
;                     const f16x8 yy = yv[m][bj];
;                     float z[8];
; #pragma unroll
;                     for (int e = 0; e < 4; ++e) { z[e] = (float)yy[e] * __builtin_amdgcn_rcpf(1.f + __builtin_amdgcn_exp2f(-LOG2E * g0[e])); z[4 + e] = (float)yy[4 + e] * __builtin_amdgcn_rcpf(1.f + __builtin_amdgcn_exp2f(-LOG2E * g1[e])); }
;                     if (br == 2) {
; #pragma unroll
;                         for (int e = 0; e < 8; ++e) z[e] += (float)za[bj][e] + (float)zb[bj][e]; }
.Lg3j_31145:
	v_cvt_f32_f16_sdwa v121, v146 dst_sel:DWORD dst_unused:UNUSED_PAD src0_sel:WORD_1
	v_cvt_f32_f16_e32 v120, v146
	v_add_f32_e32 v119, 1.0, v119
	v_rcp_f32_e32 v119, v119
	s_mov_b64 s[50:51], -1
	v_pk_mul_f32 v[114:115], v[114:115], v[120:121]
	v_cvt_f32_f16_sdwa v121, v148 dst_sel:DWORD dst_unused:UNUSED_PAD src0_sel:WORD_1
	v_cvt_f32_f16_e32 v120, v148
	s_and_b64 vcc, exec, s[38:39]
	v_pk_mul_f32 v[118:119], v[118:119], v[120:121]
	v_mul_f32_e32 v120, v40, v122
	v_mul_f32_e32 v121, v41, v123
	v_fma_f32 v120, v221, v120, v36
	v_fma_f32 v121, v221, v121, v37
	v_mul_f32_e32 v120, 0xbfb8aa3b, v120
	v_mul_f32_e32 v121, 0xbfb8aa3b, v121
	v_exp_f32_e32 v120, v120
	v_exp_f32_e32 v121, v121
	v_cvt_f32_f16_sdwa v123, v147 dst_sel:DWORD dst_unused:UNUSED_PAD src0_sel:WORD_1
	v_cvt_f32_f16_e32 v122, v147
	v_add_f32_e32 v120, 1.0, v120
	v_add_f32_e32 v121, 1.0, v121
	v_rcp_f32_e32 v120, v120
	v_rcp_f32_e32 v121, v121
	s_nop 0
	v_pk_mul_f32 v[120:121], v[120:121], v[122:123]
	s_cbranch_vccnz .LBB0_1261
	s_mov_b64 s[50:51], 0

;     __device__ __forceinline__ void operator()(const f32x4 (&acc)[2][2][4][2], const Unit& u, int wr, int wc, int fr, int fq) const {
;     ...
;         for (int ai = 0; ai < 2; ++ai) {
;             const int rowa = row0 + ai * HALF; const size_t offa = (size_t)rowa * 1024 + (size_t)(rowa >> 12) * GAPY + col0;
; #pragma unroll
;             for (int mp = 0; mp < 2; ++mp) {
;             f16x8 yv[4][2];
; #pragma unroll
;             for (int m = 2 * mp; m < 2 * mp + 2; ++m)
; #pragma unroll
;                 for (int bj = 0; bj < 2; ++bj) yv[m][bj] = *(const g_f16x8*)(Yb + offa + (size_t)m * 16 * 1024 + bj * HALF);
.LBB0_1263:
	v_cvt_pk_f16_f32 v122, v114, v115
	v_add_u32_e32 v114, 0x80, v218
	v_ashrrev_i32_e32 v115, 31, v114
	v_cvt_pk_f16_f32 v125, v116, v117
	v_lshlrev_b64 v[116:117], 10, v[114:115]
	v_cvt_pk_f16_f32 v124, v118, v119
	v_ashrrev_i32_e32 v118, 12, v114
	v_lshl_add_u64 v[114:115], v[116:117], 0, v[216:217]
	s_mov_b32 s26, 0xc00000
	v_mad_i64_i32 v[130:131], s[50:51], v118, s26, v[114:115]
	s_mov_b64 s[28:29], 0x18000
	v_lshl_add_u64 v[132:133], v[130:131], 1, s[48:49]
	v_lshl_add_u64 v[126:127], v[178:179], 0, s[28:29]
	v_cvt_pk_f16_f32 v123, v120, v121
	v_add_co_u32_e32 v114, vcc, 0x8000, v132
	global_store_dwordx4 v[126:127], v[122:125], off offset:256
	v_lshl_add_u64 v[222:223], v[228:229], 1, s[48:49]
	s_mov_b64 s[28:29], 0x50000
	v_lshl_add_u64 v[222:223], v[222:223], 0, s[28:29]
	global_load_dwordx4 v[146:149], v[222:223], off
	global_load_dwordx4 v[150:153], v[222:223], off offset:256
	v_lshl_add_u64 v[222:223], v[228:229], 1, s[48:49]
	s_mov_b64 s[28:29], 0x58000
	v_lshl_add_u64 v[222:223], v[222:223], 0, s[28:29]
	global_load_dwordx4 v[154:157], v[222:223], off
	global_load_dwordx4 v[158:161], v[222:223], off offset:256
	s_nop 0
	v_addc_co_u32_e32 v115, vcc, 0, v133, vcc
	s_nop 0
	s_and_b64 vcc, exec, s[36:37]
	s_cbranch_vccnz .LBB0_1265
	v_lshlrev_b64 v[42:43], 1, v[130:131]
	v_lshl_add_u64 v[44:45], s[40:41], 0, v[42:43]
	s_waitcnt vmcnt(6)
	v_lshl_add_u64 v[46:47], s[44:45], 0, v[42:43]
	global_load_dwordx4 v[58:61], v[44:45], off
	s_nop 0
	global_load_dwordx4 v[42:45], v[44:45], off offset:256
	s_nop 0
	global_load_dwordx4 v[66:69], v[46:47], off
	s_nop 0
	global_load_dwordx4 v[46:49], v[46:47], off offset:256
.LBB0_1265:
	v_cvt_f32_i32_e32 v134, v106
	v_cvt_f32_i32_e32 v135, v107
	v_cvt_f32_i32_e32 v110, v110
	v_cvt_f32_i32_e32 v111, v111
	v_mul_f32_e32 v107, v54, v134
	v_fma_f32 v107, v214, v107, v50
	v_mul_f32_e32 v107, 0xbfb8aa3b, v107
	v_exp_f32_e32 v107, v107
	v_cvt_f32_i32_e32 v136, v108
	v_mul_f32_e32 v106, v70, v110
	v_fma_f32 v106, v214, v106, v62
	v_add_f32_e32 v107, 1.0, v107
	v_rcp_f32_e32 v108, v107
	v_mul_f32_e32 v107, v71, v111
	v_fma_f32 v107, v214, v107, v63
	v_mul_f32_e32 v106, 0xbfb8aa3b, v106
	v_mul_f32_e32 v107, 0xbfb8aa3b, v107
	v_exp_f32_e32 v106, v106
	v_exp_f32_e32 v107, v107
	v_cvt_f32_i32_e32 v137, v109
	v_mul_f32_e32 v109, v55, v135
	v_fma_f32 v109, v214, v109, v51
	v_mul_f32_e32 v109, 0xbfb8aa3b, v109
	v_add_f32_e32 v106, 1.0, v106
	v_add_f32_e32 v107, 1.0, v107
	v_exp_f32_e32 v109, v109
	v_rcp_f32_e32 v106, v106
	v_rcp_f32_e32 v107, v107
	s_cmp_lg_u64 s[36:37], 0
	s_cbranch_scc0 .Lg3w_31289
	s_waitcnt vmcnt(11)
	s_branch .Lg3j_31289

; __device__ __forceinline__ unsigned pk2h(float lo, float hi) { f32x2 v = {lo, hi}; f16x2 h = __builtin_convertvector(v, f16x2); return __builtin_bit_cast(unsigned, h); }
;     __device__ __forceinline__ void operator()(const f32x4 (&acc)[2][2][4][2], const Unit& u, int wr, int wc, int fr, int fq) const {
;     ...
;                     f32x4 a0 = acc[ai][bj][m][0], a1 = acc[ai][bj][m][1];
;                     if constexpr (I8) { const i32x4 i0 = __builtin_bit_cast(i32x4, a0), i1 = __builtin_bit_cast(i32x4, a1);
;                         a0 = (f32x4){(float)i0.x, (float)i0.y, (float)i0.z, (float)i0.w} * sv[bj][0]; a1 = (f32x4){(float)i1.x, (float)i1.y, (float)i1.z, (float)i1.w} * sv[bj][1]; }
;                     const f32x4 g0 = a0 * rs[ai][m] + bv[bj][0], g1 = a1 * rs[ai][m] + bv[bj][1];
;                     const f16x8 yy = yv[m][bj];
;                     float z[8];
; #pragma unroll
;                     for (int e = 0; e < 4; ++e) { z[e] = (float)yy[e] * __builtin_amdgcn_rcpf(1.f + __builtin_amdgcn_exp2f(-LOG2E * g0[e])); z[4 + e] = (float)yy[4 + e] * __builtin_amdgcn_rcpf(1.f + __builtin_amdgcn_exp2f(-LOG2E * g1[e])); }
;                     if (br == 2) {
; #pragma unroll
;                         for (int e = 0; e < 8; ++e) z[e] += (float)za[bj][e] + (float)zb[bj][e]; }
;                     u32x4 w; w.x = pk2h(z[0], z[1]); w.y = pk2h(z[2], z[3]); w.z = pk2h(z[4], z[5]); w.w = pk2h(z[6], z[7]);
;                     f16* dst = (br == 2) ? merged : Yb;
;                     gst16(dst + off + bj * HALF, w); } } } }
.Lg3j_31289:
	v_cvt_f32_f16_sdwa v111, v174 dst_sel:DWORD dst_unused:UNUSED_PAD src0_sel:WORD_1
	v_cvt_f32_f16_e32 v110, v174
	v_add_f32_e32 v109, 1.0, v109
	v_rcp_f32_e32 v109, v109
	v_cvt_f32_i32_e32 v112, v112
	v_pk_mul_f32 v[106:107], v[106:107], v[110:111]
	v_cvt_f32_f16_sdwa v111, v176 dst_sel:DWORD dst_unused:UNUSED_PAD src0_sel:WORD_1
	v_cvt_f32_f16_e32 v110, v176
	v_cvt_f32_i32_e32 v113, v113
	v_cvt_f32_f16_sdwa v135, v175 dst_sel:DWORD dst_unused:UNUSED_PAD src0_sel:WORD_1
	v_cvt_f32_f16_e32 v134, v175
	v_pk_mul_f32 v[108:109], v[108:109], v[110:111]
	v_mul_f32_e32 v111, v56, v136
	v_fma_f32 v111, v214, v111, v52
	v_mul_f32_e32 v111, 0xbfb8aa3b, v111
	v_exp_f32_e32 v111, v111
	v_mul_f32_e32 v110, v72, v112
	v_fma_f32 v110, v214, v110, v64
	v_mul_f32_e32 v110, 0xbfb8aa3b, v110
	v_add_f32_e32 v111, 1.0, v111
	v_rcp_f32_e32 v112, v111
	v_mul_f32_e32 v111, v73, v113
	v_mul_f32_e32 v113, v57, v137
	v_fma_f32 v111, v214, v111, v65
	v_fma_f32 v113, v214, v113, v53
	v_mul_f32_e32 v111, 0xbfb8aa3b, v111
	v_mul_f32_e32 v113, 0xbfb8aa3b, v113
	v_exp_f32_e32 v110, v110
	v_exp_f32_e32 v111, v111
	v_exp_f32_e32 v113, v113
	v_cvt_f32_f16_sdwa v127, v177 dst_sel:DWORD dst_unused:UNUSED_PAD src0_sel:WORD_1
	v_add_f32_e32 v110, 1.0, v110
	v_add_f32_e32 v111, 1.0, v111
	v_add_f32_e32 v113, 1.0, v113
	v_rcp_f32_e32 v110, v110
	v_rcp_f32_e32 v111, v111
	v_rcp_f32_e32 v113, v113
	v_cvt_f32_f16_e32 v126, v177
	s_and_b64 vcc, exec, s[36:37]
	v_pk_mul_f32 v[110:111], v[110:111], v[134:135]
	v_pk_mul_f32 v[112:113], v[112:113], v[126:127]
	s_cbranch_vccnz .LBB0_1267
	v_cvt_f32_f16_sdwa v127, v58 dst_sel:DWORD dst_unused:UNUSED_PAD src0_sel:WORD_1
	v_cvt_f32_f16_e32 v126, v58
	s_waitcnt vmcnt(1)
	v_cvt_f32_f16_sdwa v129, v66 dst_sel:DWORD dst_unused:UNUSED_PAD src0_sel:WORD_1
	v_cvt_f32_f16_e32 v128, v66
	v_cvt_f32_f16_sdwa v135, v59 dst_sel:DWORD dst_unused:UNUSED_PAD src0_sel:WORD_1
	v_cvt_f32_f16_e32 v134, v59
	v_cvt_f32_f16_sdwa v137, v67 dst_sel:DWORD dst_unused:UNUSED_PAD src0_sel:WORD_1
	v_cvt_f32_f16_e32 v136, v67
	v_cvt_f32_f16_sdwa v139, v60 dst_sel:DWORD dst_unused:UNUSED_PAD src0_sel:WORD_1
	v_cvt_f32_f16_e32 v138, v60
	v_cvt_f32_f16_sdwa v141, v68 dst_sel:DWORD dst_unused:UNUSED_PAD src0_sel:WORD_1
	v_cvt_f32_f16_e32 v140, v68
	v_cvt_f32_f16_sdwa v143, v61 dst_sel:DWORD dst_unused:UNUSED_PAD src0_sel:WORD_1
	v_cvt_f32_f16_e32 v142, v61
	v_cvt_f32_f16_sdwa v145, v69 dst_sel:DWORD dst_unused:UNUSED_PAD src0_sel:WORD_1
	v_cvt_f32_f16_e32 v144, v69
	v_pk_add_f32 v[126:127], v[128:129], v[126:127]
	v_pk_add_f32 v[128:129], v[136:137], v[134:135]
	v_pk_add_f32 v[134:135], v[140:141], v[138:139]
	v_pk_add_f32 v[136:137], v[144:145], v[142:143]
	v_pk_add_f32 v[106:107], v[106:107], v[126:127]
	v_pk_add_f32 v[110:111], v[110:111], v[128:129]
	v_pk_add_f32 v[108:109], v[108:109], v[134:135]
	v_pk_add_f32 v[112:113], v[112:113], v[136:137]
.LBB0_1267:
	v_cvt_pk_f16_f32 v128, v108, v109
	v_cvt_f32_i32_e32 v108, v104
	v_cvt_f32_i32_e32 v104, v98
	v_cvt_pk_f16_f32 v127, v110, v111
	v_cvt_f32_i32_e32 v110, v99
	v_cvt_f32_i32_e32 v102, v102
	v_mul_f32_e32 v99, v30, v104
	v_fma_f32 v99, v214, v99, v26
	v_mul_f32_e32 v99, 0xbfb8aa3b, v99
	v_exp_f32_e32 v99, v99
	v_cvt_f32_i32_e32 v103, v103
	v_mul_f32_e32 v98, v38, v102
	v_fma_f32 v98, v214, v98, v34
	v_add_f32_e32 v99, 1.0, v99
	v_rcp_f32_e32 v102, v99
	v_mul_f32_e32 v99, v39, v103
	v_fma_f32 v99, v214, v99, v35
	v_mul_f32_e32 v98, 0xbfb8aa3b, v98
	v_mul_f32_e32 v99, 0xbfb8aa3b, v99
	v_exp_f32_e32 v98, v98
	v_exp_f32_e32 v99, v99
	v_mul_f32_e32 v103, v31, v110
	v_fma_f32 v103, v214, v103, v27
	v_mul_f32_e32 v103, 0xbfb8aa3b, v103
	v_add_f32_e32 v98, 1.0, v98
	v_add_f32_e32 v99, 1.0, v99
	v_exp_f32_e32 v103, v103
	v_cvt_f32_i32_e32 v109, v105
	v_rcp_f32_e32 v98, v98
	v_rcp_f32_e32 v99, v99
	s_cmp_lg_u64 s[36:37], 0
	s_cbranch_scc0 .Lg3w_31389
	s_waitcnt vmcnt(10)
	s_branch .Lg3j_31389

; __device__ __forceinline__ unsigned pk2h(float lo, float hi) { f32x2 v = {lo, hi}; f16x2 h = __builtin_convertvector(v, f16x2); return __builtin_bit_cast(unsigned, h); }
;     __device__ __forceinline__ void operator()(const f32x4 (&acc)[2][2][4][2], const Unit& u, int wr, int wc, int fr, int fq) const {
;     ...
;                     f32x4 a0 = acc[ai][bj][m][0], a1 = acc[ai][bj][m][1];
;                     if constexpr (I8) { const i32x4 i0 = __builtin_bit_cast(i32x4, a0), i1 = __builtin_bit_cast(i32x4, a1);
;                         a0 = (f32x4){(float)i0.x, (float)i0.y, (float)i0.z, (float)i0.w} * sv[bj][0]; a1 = (f32x4){(float)i1.x, (float)i1.y, (float)i1.z, (float)i1.w} * sv[bj][1]; }
;                     const f32x4 g0 = a0 * rs[ai][m] + bv[bj][0], g1 = a1 * rs[ai][m] + bv[bj][1];
;                     const f16x8 yy = yv[m][bj];
;                     float z[8];
; #pragma unroll
;                     for (int e = 0; e < 4; ++e) { z[e] = (float)yy[e] * __builtin_amdgcn_rcpf(1.f + __builtin_amdgcn_exp2f(-LOG2E * g0[e])); z[4 + e] = (float)yy[4 + e] * __builtin_amdgcn_rcpf(1.f + __builtin_amdgcn_exp2f(-LOG2E * g1[e])); }
;                     if (br == 2) {
; #pragma unroll
;                         for (int e = 0; e < 8; ++e) z[e] += (float)za[bj][e] + (float)zb[bj][e]; }
;                     u32x4 w; w.x = pk2h(z[0], z[1]); w.y = pk2h(z[2], z[3]); w.z = pk2h(z[4], z[5]); w.w = pk2h(z[6], z[7]);
;                     f16* dst = (br == 2) ? merged : Yb;
;                     gst16(dst + off + bj * HALF, w); } } } }
.Lg3j_31389:
	v_cvt_f32_f16_sdwa v105, v180 dst_sel:DWORD dst_unused:UNUSED_PAD src0_sel:WORD_1
	v_cvt_f32_f16_e32 v104, v180
	v_add_f32_e32 v103, 1.0, v103
	v_rcp_f32_e32 v103, v103
	v_cvt_pk_f16_f32 v126, v106, v107
	v_pk_mul_f32 v[98:99], v[98:99], v[104:105]
	v_cvt_f32_f16_sdwa v105, v182 dst_sel:DWORD dst_unused:UNUSED_PAD src0_sel:WORD_1
	v_cvt_f32_f16_e32 v104, v182
	v_cvt_pk_f16_f32 v129, v112, v113
	v_lshl_add_u64 v[106:107], v[130:131], 1, s[46:47]
	s_mov_b64 s[46:47], -1
	v_pk_mul_f32 v[102:103], v[102:103], v[104:105]
	v_mul_f32_e32 v104, v40, v108
	v_mul_f32_e32 v105, v41, v109
	v_fma_f32 v104, v214, v104, v36
	v_fma_f32 v105, v214, v105, v37
	v_mul_f32_e32 v104, 0xbfb8aa3b, v104
	v_mul_f32_e32 v105, 0xbfb8aa3b, v105
	v_exp_f32_e32 v104, v104
	v_exp_f32_e32 v105, v105
	v_cvt_f32_f16_sdwa v109, v181 dst_sel:DWORD dst_unused:UNUSED_PAD src0_sel:WORD_1
	v_cvt_f32_f16_e32 v108, v181
	v_add_f32_e32 v104, 1.0, v104
	v_add_f32_e32 v105, 1.0, v105
	v_rcp_f32_e32 v104, v104
	v_rcp_f32_e32 v105, v105
	s_and_b64 vcc, exec, s[38:39]
	global_store_dwordx4 v[106:107], v[126:129], off
	v_pk_mul_f32 v[104:105], v[104:105], v[108:109]
	s_cbranch_vccnz .LBB0_1269
	s_mov_b64 s[46:47], 0
.LBB0_1269:
	v_cvt_f32_i32_e32 v100, v100
	v_cvt_f32_i32_e32 v101, v101
	v_cvt_f32_f16_sdwa v109, v183 dst_sel:DWORD dst_unused:UNUSED_PAD src0_sel:WORD_1
	v_cvt_f32_f16_e32 v108, v183
	v_mul_f32_e32 v100, v32, v100
	v_mul_f32_e32 v101, v33, v101
	v_fma_f32 v100, v214, v100, v28
	v_fma_f32 v101, v214, v101, v29
	v_mul_f32_e32 v100, 0xbfb8aa3b, v100
	v_mul_f32_e32 v101, 0xbfb8aa3b, v101
	v_exp_f32_e32 v100, v100
	v_exp_f32_e32 v101, v101
	s_andn2_b64 vcc, exec, s[46:47]
	v_add_f32_e32 v100, 1.0, v100
	v_add_f32_e32 v101, 1.0, v101
	v_rcp_f32_e32 v100, v100
	v_rcp_f32_e32 v101, v101
	s_nop 0
	v_pk_mul_f32 v[100:101], v[100:101], v[108:109]
	s_cbranch_vccnz .LBB0_1271
	v_cvt_f32_f16_sdwa v109, v42 dst_sel:DWORD dst_unused:UNUSED_PAD src0_sel:WORD_1
	v_cvt_f32_f16_e32 v108, v42
	s_waitcnt vmcnt(1)
	v_cvt_f32_f16_sdwa v111, v46 dst_sel:DWORD dst_unused:UNUSED_PAD src0_sel:WORD_1
	v_cvt_f32_f16_e32 v110, v46
	v_cvt_f32_f16_sdwa v113, v43 dst_sel:DWORD dst_unused:UNUSED_PAD src0_sel:WORD_1
	v_cvt_f32_f16_e32 v112, v43
	v_cvt_f32_f16_sdwa v123, v47 dst_sel:DWORD dst_unused:UNUSED_PAD src0_sel:WORD_1
	v_cvt_f32_f16_e32 v122, v47
	v_cvt_f32_f16_sdwa v125, v44 dst_sel:DWORD dst_unused:UNUSED_PAD src0_sel:WORD_1
	v_cvt_f32_f16_e32 v124, v44
	v_cvt_f32_f16_sdwa v127, v48 dst_sel:DWORD dst_unused:UNUSED_PAD src0_sel:WORD_1
	v_cvt_f32_f16_e32 v126, v48
	v_cvt_f32_f16_sdwa v129, v45 dst_sel:DWORD dst_unused:UNUSED_PAD src0_sel:WORD_1
	v_cvt_f32_f16_e32 v128, v45
	v_cvt_f32_f16_sdwa v135, v49 dst_sel:DWORD dst_unused:UNUSED_PAD src0_sel:WORD_1
	v_cvt_f32_f16_e32 v134, v49
	v_pk_add_f32 v[108:109], v[110:111], v[108:109]
	v_pk_add_f32 v[110:111], v[122:123], v[112:113]
	v_pk_add_f32 v[112:113], v[126:127], v[124:125]
	v_pk_add_f32 v[122:123], v[134:135], v[128:129]
	v_pk_add_f32 v[98:99], v[98:99], v[108:109]
	v_pk_add_f32 v[104:105], v[104:105], v[110:111]
	v_pk_add_f32 v[102:103], v[102:103], v[112:113]
	v_pk_add_f32 v[100:101], v[100:101], v[122:123]

;     __device__ __forceinline__ void operator()(const f32x4 (&acc)[2][2][4][2], const Unit& u, int wr, int wc, int fr, int fq) const {
;     ...
;                     f32x4 a0 = acc[ai][bj][m][0], a1 = acc[ai][bj][m][1];
;                     if constexpr (I8) { const i32x4 i0 = __builtin_bit_cast(i32x4, a0), i1 = __builtin_bit_cast(i32x4, a1);
;                         a0 = (f32x4){(float)i0.x, (float)i0.y, (float)i0.z, (float)i0.w} * sv[bj][0]; a1 = (f32x4){(float)i1.x, (float)i1.y, (float)i1.z, (float)i1.w} * sv[bj][1]; }
;                     const f32x4 g0 = a0 * rs[ai][m] + bv[bj][0], g1 = a1 * rs[ai][m] + bv[bj][1];
;                     const f16x8 yy = yv[m][bj];
;                     float z[8];
; #pragma unroll
;                     for (int e = 0; e < 4; ++e) { z[e] = (float)yy[e] * __builtin_amdgcn_rcpf(1.f + __builtin_amdgcn_exp2f(-LOG2E * g0[e])); z[4 + e] = (float)yy[4 + e] * __builtin_amdgcn_rcpf(1.f + __builtin_amdgcn_exp2f(-LOG2E * g1[e])); }
.LBB0_1273:
	v_cvt_f32_i32_e32 v98, v90
	v_cvt_f32_i32_e32 v99, v91
	v_cvt_f32_i32_e32 v94, v94
	v_cvt_f32_i32_e32 v95, v95
	v_mul_f32_e32 v91, v54, v98
	v_fma_f32 v91, v215, v91, v50
	v_mul_f32_e32 v91, 0xbfb8aa3b, v91
	v_exp_f32_e32 v91, v91
	v_cvt_f32_i32_e32 v100, v92
	v_mul_f32_e32 v90, v70, v94
	v_fma_f32 v90, v215, v90, v62
	v_add_f32_e32 v91, 1.0, v91
	v_rcp_f32_e32 v92, v91
	v_mul_f32_e32 v91, v71, v95
	v_fma_f32 v91, v215, v91, v63
	v_mul_f32_e32 v90, 0xbfb8aa3b, v90
	v_mul_f32_e32 v91, 0xbfb8aa3b, v91
	v_exp_f32_e32 v90, v90
	v_exp_f32_e32 v91, v91
	v_cvt_f32_i32_e32 v101, v93
	v_mul_f32_e32 v93, v55, v99
	v_fma_f32 v93, v215, v93, v51
	v_mul_f32_e32 v93, 0xbfb8aa3b, v93
	v_add_f32_e32 v90, 1.0, v90
	v_add_f32_e32 v91, 1.0, v91
	v_exp_f32_e32 v93, v93
	v_rcp_f32_e32 v90, v90
	v_rcp_f32_e32 v91, v91
	s_cmp_lg_u64 s[36:37], 0
	s_cbranch_scc0 .Lg3w_31519
	s_waitcnt vmcnt(9)
	s_branch .Lg3j_31519

; __device__ __forceinline__ unsigned pk2h(float lo, float hi) { f32x2 v = {lo, hi}; f16x2 h = __builtin_convertvector(v, f16x2); return __builtin_bit_cast(unsigned, h); }
;     __device__ __forceinline__ void operator()(const f32x4 (&acc)[2][2][4][2], const Unit& u, int wr, int wc, int fr, int fq) const {
;     ...
;                     f32x4 a0 = acc[ai][bj][m][0], a1 = acc[ai][bj][m][1];
;                     if constexpr (I8) { const i32x4 i0 = __builtin_bit_cast(i32x4, a0), i1 = __builtin_bit_cast(i32x4, a1);
;                         a0 = (f32x4){(float)i0.x, (float)i0.y, (float)i0.z, (float)i0.w} * sv[bj][0]; a1 = (f32x4){(float)i1.x, (float)i1.y, (float)i1.z, (float)i1.w} * sv[bj][1]; }
;                     const f32x4 g0 = a0 * rs[ai][m] + bv[bj][0], g1 = a1 * rs[ai][m] + bv[bj][1];
;                     const f16x8 yy = yv[m][bj];
;                     float z[8];
; #pragma unroll
;                     for (int e = 0; e < 4; ++e) { z[e] = (float)yy[e] * __builtin_amdgcn_rcpf(1.f + __builtin_amdgcn_exp2f(-LOG2E * g0[e])); z[4 + e] = (float)yy[4 + e] * __builtin_amdgcn_rcpf(1.f + __builtin_amdgcn_exp2f(-LOG2E * g1[e])); }
;                     if (br == 2) {
; #pragma unroll
;                         for (int e = 0; e < 8; ++e) z[e] += (float)za[bj][e] + (float)zb[bj][e]; }
;                     u32x4 w; w.x = pk2h(z[0], z[1]); w.y = pk2h(z[2], z[3]); w.z = pk2h(z[4], z[5]); w.w = pk2h(z[6], z[7]);
;                     f16* dst = (br == 2) ? merged : Yb;
;                     gst16(dst + off + bj * HALF, w); } } } }
.Lg3j_31519:
	v_cvt_f32_f16_sdwa v95, v162 dst_sel:DWORD dst_unused:UNUSED_PAD src0_sel:WORD_1
	v_cvt_f32_f16_e32 v94, v162
	v_add_f32_e32 v93, 1.0, v93
	v_rcp_f32_e32 v93, v93
	v_cvt_f32_i32_e32 v96, v96
	v_pk_mul_f32 v[90:91], v[90:91], v[94:95]
	v_cvt_f32_f16_sdwa v95, v164 dst_sel:DWORD dst_unused:UNUSED_PAD src0_sel:WORD_1
	v_cvt_f32_f16_e32 v94, v164
	v_cvt_f32_i32_e32 v97, v97
	v_cvt_f32_f16_sdwa v99, v163 dst_sel:DWORD dst_unused:UNUSED_PAD src0_sel:WORD_1
	v_cvt_f32_f16_e32 v98, v163
	v_pk_mul_f32 v[92:93], v[92:93], v[94:95]
	v_mul_f32_e32 v95, v56, v100
	v_fma_f32 v95, v215, v95, v52
	v_mul_f32_e32 v95, 0xbfb8aa3b, v95
	v_exp_f32_e32 v95, v95
	v_mul_f32_e32 v94, v72, v96
	v_fma_f32 v94, v215, v94, v64
	v_mul_f32_e32 v94, 0xbfb8aa3b, v94
	v_add_f32_e32 v95, 1.0, v95
	v_rcp_f32_e32 v96, v95
	v_mul_f32_e32 v95, v73, v97
	v_fma_f32 v95, v215, v95, v65
	v_mul_f32_e32 v95, 0xbfb8aa3b, v95
	v_exp_f32_e32 v94, v94
	v_exp_f32_e32 v95, v95
	v_mul_f32_e32 v97, v57, v101
	v_fma_f32 v97, v215, v97, v53
	v_mul_f32_e32 v97, 0xbfb8aa3b, v97
	v_add_f32_e32 v94, 1.0, v94
	v_add_f32_e32 v95, 1.0, v95
	v_exp_f32_e32 v97, v97
	v_rcp_f32_e32 v94, v94
	v_rcp_f32_e32 v95, v95
	s_and_b64 vcc, exec, s[36:37]
	v_add_f32_e32 v97, 1.0, v97
	v_rcp_f32_e32 v97, v97
	v_pk_mul_f32 v[94:95], v[94:95], v[98:99]
	v_cvt_f32_f16_sdwa v99, v165 dst_sel:DWORD dst_unused:UNUSED_PAD src0_sel:WORD_1
	v_cvt_f32_f16_e32 v98, v165
	v_pk_mul_f32 v[96:97], v[96:97], v[98:99]
	s_cbranch_vccnz .LBB0_1275
	v_cvt_f32_f16_sdwa v99, v58 dst_sel:DWORD dst_unused:UNUSED_PAD src0_sel:WORD_1
	v_cvt_f32_f16_e32 v98, v58
	s_waitcnt vmcnt(1)
	v_cvt_f32_f16_sdwa v101, v66 dst_sel:DWORD dst_unused:UNUSED_PAD src0_sel:WORD_1
	v_cvt_f32_f16_e32 v100, v66
	v_cvt_f32_f16_sdwa v103, v59 dst_sel:DWORD dst_unused:UNUSED_PAD src0_sel:WORD_1
	v_cvt_f32_f16_e32 v102, v59
	v_cvt_f32_f16_sdwa v105, v67 dst_sel:DWORD dst_unused:UNUSED_PAD src0_sel:WORD_1
	v_cvt_f32_f16_e32 v104, v67
	v_cvt_f32_f16_sdwa v109, v60 dst_sel:DWORD dst_unused:UNUSED_PAD src0_sel:WORD_1
	v_cvt_f32_f16_e32 v108, v60
	v_cvt_f32_f16_sdwa v111, v68 dst_sel:DWORD dst_unused:UNUSED_PAD src0_sel:WORD_1
	v_cvt_f32_f16_e32 v110, v68
	v_cvt_f32_f16_sdwa v113, v61 dst_sel:DWORD dst_unused:UNUSED_PAD src0_sel:WORD_1
	v_cvt_f32_f16_e32 v112, v61
	v_cvt_f32_f16_sdwa v119, v69 dst_sel:DWORD dst_unused:UNUSED_PAD src0_sel:WORD_1
	v_cvt_f32_f16_e32 v118, v69
	v_pk_add_f32 v[98:99], v[100:101], v[98:99]
	v_pk_add_f32 v[100:101], v[104:105], v[102:103]
	v_pk_add_f32 v[102:103], v[110:111], v[108:109]
	v_pk_add_f32 v[104:105], v[118:119], v[112:113]
	v_pk_add_f32 v[90:91], v[90:91], v[98:99]
	v_pk_add_f32 v[94:95], v[94:95], v[100:101]
	v_pk_add_f32 v[92:93], v[92:93], v[102:103]
	v_pk_add_f32 v[96:97], v[96:97], v[104:105]
.LBB0_1275:
	s_mov_b32 s26, 0x8000
	v_cvt_pk_f16_f32 v90, v90, v91
	v_cvt_pk_f16_f32 v91, v94, v95
	v_add_co_u32_e32 v94, vcc, s26, v106
	v_cvt_pk_f16_f32 v92, v92, v93
	v_cvt_pk_f16_f32 v93, v96, v97
	v_addc_co_u32_e32 v95, vcc, 0, v107, vcc
	global_store_dwordx4 v[94:95], v[90:93], off
	v_cvt_f32_i32_e32 v86, v86
	v_cvt_f32_i32_e32 v87, v87
	v_cvt_f32_i32_e32 v90, v88
	v_cvt_f32_i32_e32 v88, v82
	v_cvt_f32_i32_e32 v92, v83
	v_mul_f32_e32 v82, v38, v86
	v_fma_f32 v82, v215, v82, v34
	v_mul_f32_e32 v83, v30, v88
	v_fma_f32 v83, v215, v83, v26
	v_mul_f32_e32 v83, 0xbfb8aa3b, v83
	v_exp_f32_e32 v83, v83
	v_mul_f32_e32 v82, 0xbfb8aa3b, v82
	v_exp_f32_e32 v82, v82
	v_cvt_f32_i32_e32 v91, v89
	v_add_f32_e32 v83, 1.0, v83
	v_rcp_f32_e32 v86, v83
	v_mul_f32_e32 v83, v39, v87
	v_fma_f32 v83, v215, v83, v35
	v_mul_f32_e32 v83, 0xbfb8aa3b, v83
	v_exp_f32_e32 v83, v83
	v_mul_f32_e32 v87, v31, v92
	v_fma_f32 v87, v215, v87, v27
	v_mul_f32_e32 v87, 0xbfb8aa3b, v87
	v_add_f32_e32 v82, 1.0, v82
	v_add_f32_e32 v83, 1.0, v83
	v_exp_f32_e32 v87, v87
	v_rcp_f32_e32 v82, v82
	v_rcp_f32_e32 v83, v83
	s_cmp_lg_u64 s[36:37], 0
	s_cbranch_scc0 .Lg3w_31625
	s_waitcnt vmcnt(9)
	s_branch .Lg3j_31625

;     __device__ __forceinline__ void operator()(const f32x4 (&acc)[2][2][4][2], const Unit& u, int wr, int wc, int fr, int fq) const {
;     ...
;             const int rowa = row0 + ai * HALF; const size_t offa = (size_t)rowa * 1024 + (size_t)(rowa >> 12) * GAPY + col0;
; #pragma unroll
;             for (int mp = 0; mp < 2; ++mp) {
;             f16x8 yv[4][2];
; #pragma unroll
;             for (int m = 2 * mp; m < 2 * mp + 2; ++m)
; #pragma unroll
;                 for (int bj = 0; bj < 2; ++bj) yv[m][bj] = *(const g_f16x8*)(Yb + offa + (size_t)m * 16 * 1024 + bj * HALF);
; #pragma unroll
;             for (int m = 2 * mp; m < 2 * mp + 2; ++m) { const size_t off = offa + (size_t)m * 16 * 1024;
;                 f16x8 za[2], zb[2];
;                 if (br == 2) {
; #pragma unroll
;                     for (int bj = 0; bj < 2; ++bj) { za[bj] = *(const g_f16x8*)(Y + off + bj * HALF); zb[bj] = *(const g_f16x8*)(Y + YSTR + off + bj * HALF); } }
; #pragma unroll
;                 for (int bj = 0; bj < 2; ++bj) {
;                     f32x4 a0 = acc[ai][bj][m][0], a1 = acc[ai][bj][m][1];
;                     if constexpr (I8) { const i32x4 i0 = __builtin_bit_cast(i32x4, a0), i1 = __builtin_bit_cast(i32x4, a1);
;                         a0 = (f32x4){(float)i0.x, (float)i0.y, (float)i0.z, (float)i0.w} * sv[bj][0]; a1 = (f32x4){(float)i1.x, (float)i1.y, (float)i1.z, (float)i1.w} * sv[bj][1]; }
;                     const f32x4 g0 = a0 * rs[ai][m] + bv[bj][0], g1 = a1 * rs[ai][m] + bv[bj][1];
;                     const f16x8 yy = yv[m][bj];
;                     float z[8];
; #pragma unroll
;                     for (int e = 0; e < 4; ++e) { z[e] = (float)yy[e] * __builtin_amdgcn_rcpf(1.f + __builtin_amdgcn_exp2f(-LOG2E * g0[e])); z[4 + e] = (float)yy[4 + e] * __builtin_amdgcn_rcpf(1.f + __builtin_amdgcn_exp2f(-LOG2E * g1[e])); }
;                     if (br == 2) {
; #pragma unroll
;                         for (int e = 0; e < 8; ++e) z[e] += (float)za[bj][e] + (float)zb[bj][e]; }
;                     u32x4 w; w.x = pk2h(z[0], z[1]); w.y = pk2h(z[2], z[3]); w.z = pk2h(z[4], z[5]); w.w = pk2h(z[6], z[7]);
;                     f16* dst = (br == 2) ? merged : Yb;
;                     gst16(dst + off + bj * HALF, w); } } } }
.Lg3j_31625:
	v_cvt_f32_f16_sdwa v89, v166 dst_sel:DWORD dst_unused:UNUSED_PAD src0_sel:WORD_1
	v_cvt_f32_f16_e32 v88, v166
	v_add_f32_e32 v87, 1.0, v87
	v_rcp_f32_e32 v87, v87
	s_mov_b64 s[46:47], -1
	v_pk_mul_f32 v[82:83], v[82:83], v[88:89]
	v_cvt_f32_f16_sdwa v89, v168 dst_sel:DWORD dst_unused:UNUSED_PAD src0_sel:WORD_1
	v_cvt_f32_f16_e32 v88, v168
	s_and_b64 vcc, exec, s[38:39]
	v_pk_mul_f32 v[86:87], v[86:87], v[88:89]
	v_mul_f32_e32 v88, v40, v90
	v_mul_f32_e32 v89, v41, v91
	v_fma_f32 v88, v215, v88, v36
	v_fma_f32 v89, v215, v89, v37
	v_mul_f32_e32 v88, 0xbfb8aa3b, v88
	v_mul_f32_e32 v89, 0xbfb8aa3b, v89
	v_exp_f32_e32 v88, v88
	v_exp_f32_e32 v89, v89
	v_cvt_f32_f16_sdwa v91, v167 dst_sel:DWORD dst_unused:UNUSED_PAD src0_sel:WORD_1
	v_cvt_f32_f16_e32 v90, v167
	v_add_f32_e32 v88, 1.0, v88
	v_add_f32_e32 v89, 1.0, v89
	v_rcp_f32_e32 v88, v88
	v_rcp_f32_e32 v89, v89
	s_nop 0
	v_pk_mul_f32 v[88:89], v[88:89], v[90:91]
	s_cbranch_vccnz .LBB0_1277
	s_mov_b64 s[46:47], 0
.LBB0_1277:
	v_cvt_f32_i32_e32 v84, v84
	v_cvt_f32_i32_e32 v85, v85
	v_cvt_f32_f16_sdwa v91, v169 dst_sel:DWORD dst_unused:UNUSED_PAD src0_sel:WORD_1
	v_cvt_f32_f16_e32 v90, v169
	v_mul_f32_e32 v84, v32, v84
	v_mul_f32_e32 v85, v33, v85
	v_fma_f32 v84, v215, v84, v28
	v_fma_f32 v85, v215, v85, v29
	v_mul_f32_e32 v84, 0xbfb8aa3b, v84
	v_mul_f32_e32 v85, 0xbfb8aa3b, v85
	v_exp_f32_e32 v84, v84
	v_exp_f32_e32 v85, v85
	s_andn2_b64 vcc, exec, s[46:47]
	v_add_f32_e32 v84, 1.0, v84
	v_add_f32_e32 v85, 1.0, v85
	v_rcp_f32_e32 v84, v84
	v_rcp_f32_e32 v85, v85
	s_nop 0
	v_pk_mul_f32 v[84:85], v[84:85], v[90:91]
	s_cbranch_vccnz .LBB0_1279
	v_cvt_f32_f16_sdwa v91, v42 dst_sel:DWORD dst_unused:UNUSED_PAD src0_sel:WORD_1
	v_cvt_f32_f16_e32 v90, v42
	s_waitcnt vmcnt(1)
	v_cvt_f32_f16_sdwa v93, v46 dst_sel:DWORD dst_unused:UNUSED_PAD src0_sel:WORD_1
	v_cvt_f32_f16_e32 v92, v46
	v_cvt_f32_f16_sdwa v95, v43 dst_sel:DWORD dst_unused:UNUSED_PAD src0_sel:WORD_1
	v_cvt_f32_f16_e32 v94, v43
	v_cvt_f32_f16_sdwa v97, v47 dst_sel:DWORD dst_unused:UNUSED_PAD src0_sel:WORD_1
	v_cvt_f32_f16_e32 v96, v47
	v_cvt_f32_f16_sdwa v99, v44 dst_sel:DWORD dst_unused:UNUSED_PAD src0_sel:WORD_1
	v_cvt_f32_f16_e32 v98, v44
	v_cvt_f32_f16_sdwa v101, v48 dst_sel:DWORD dst_unused:UNUSED_PAD src0_sel:WORD_1
	v_cvt_f32_f16_e32 v100, v48
	v_cvt_f32_f16_sdwa v103, v45 dst_sel:DWORD dst_unused:UNUSED_PAD src0_sel:WORD_1
	v_cvt_f32_f16_e32 v102, v45
	v_cvt_f32_f16_sdwa v105, v49 dst_sel:DWORD dst_unused:UNUSED_PAD src0_sel:WORD_1
	v_cvt_f32_f16_e32 v104, v49
	v_pk_add_f32 v[90:91], v[92:93], v[90:91]
	v_pk_add_f32 v[92:93], v[96:97], v[94:95]
	v_pk_add_f32 v[94:95], v[100:101], v[98:99]
	v_pk_add_f32 v[96:97], v[104:105], v[102:103]
	v_pk_add_f32 v[82:83], v[82:83], v[90:91]
	v_pk_add_f32 v[88:89], v[88:89], v[92:93]
	v_pk_add_f32 v[86:87], v[86:87], v[94:95]
	v_pk_add_f32 v[84:85], v[84:85], v[96:97]
.LBB0_1279:
	s_mov_b64 s[28:29], 0x8000
	v_lshl_add_u64 v[94:95], v[106:107], 0, s[28:29]
	v_cvt_pk_f16_f32 v90, v82, v83
	v_cvt_pk_f16_f32 v91, v88, v89
	v_cvt_pk_f16_f32 v92, v86, v87
	v_cvt_pk_f16_f32 v93, v84, v85
	v_add_co_u32_e32 v82, vcc, 0x10000, v132
	global_store_dwordx4 v[94:95], v[90:93], off offset:256
	s_nop 0
	v_addc_co_u32_e32 v83, vcc, 0, v133, vcc
	v_add_co_u32_e32 v82, vcc, 0x18000, v132
	s_nop 1
	v_addc_co_u32_e32 v83, vcc, 0, v133, vcc
	s_nop 0
	s_and_b64 vcc, exec, s[36:37]
	s_cbranch_vccnz .LBB0_1281
	v_mov_b64_e32 v[42:43], 0x10000
	v_lshl_add_u64 v[42:43], v[130:131], 1, v[42:43]
	v_lshl_add_u64 v[44:45], s[40:41], 0, v[42:43]
	s_waitcnt vmcnt(2)
	v_lshl_add_u64 v[46:47], s[44:45], 0, v[42:43]
	global_load_dwordx4 v[58:61], v[44:45], off
	s_nop 0
	global_load_dwordx4 v[42:45], v[44:45], off offset:256
	s_nop 0
	global_load_dwordx4 v[66:69], v[46:47], off
	s_nop 0
	global_load_dwordx4 v[46:49], v[46:47], off offset:256
.LBB0_1281:
	v_cvt_f32_i32_e32 v98, v74
	v_cvt_f32_i32_e32 v99, v75
	v_cvt_f32_i32_e32 v78, v78
	v_cvt_f32_i32_e32 v79, v79
	v_mul_f32_e32 v75, v54, v98
	v_fma_f32 v75, v212, v75, v50
	v_mul_f32_e32 v75, 0xbfb8aa3b, v75
	v_exp_f32_e32 v75, v75
	v_cvt_f32_i32_e32 v100, v76
	v_mul_f32_e32 v74, v70, v78
	v_fma_f32 v74, v212, v74, v62
	v_add_f32_e32 v75, 1.0, v75
	v_rcp_f32_e32 v76, v75
	v_mul_f32_e32 v75, v71, v79
	v_fma_f32 v75, v212, v75, v63
	v_mul_f32_e32 v74, 0xbfb8aa3b, v74
	v_mul_f32_e32 v75, 0xbfb8aa3b, v75
	v_exp_f32_e32 v74, v74
	v_exp_f32_e32 v75, v75
	v_cvt_f32_i32_e32 v101, v77
	v_mul_f32_e32 v77, v55, v99
	v_fma_f32 v77, v212, v77, v51
	v_mul_f32_e32 v77, 0xbfb8aa3b, v77
	v_add_f32_e32 v74, 1.0, v74
	v_add_f32_e32 v75, 1.0, v75
	v_exp_f32_e32 v77, v77
	v_rcp_f32_e32 v74, v74
	v_rcp_f32_e32 v75, v75
	s_cmp_lg_u64 s[36:37], 0
	s_cbranch_scc0 .Lg3w_31765
	s_waitcnt vmcnt(7)
	s_branch .Lg3j_31765

; __device__ __forceinline__ unsigned pk2h(float lo, float hi) { f32x2 v = {lo, hi}; f16x2 h = __builtin_convertvector(v, f16x2); return __builtin_bit_cast(unsigned, h); }
;     __device__ __forceinline__ void operator()(const f32x4 (&acc)[2][2][4][2], const Unit& u, int wr, int wc, int fr, int fq) const {
;     ...
;                     f32x4 a0 = acc[ai][bj][m][0], a1 = acc[ai][bj][m][1];
;                     if constexpr (I8) { const i32x4 i0 = __builtin_bit_cast(i32x4, a0), i1 = __builtin_bit_cast(i32x4, a1);
;                         a0 = (f32x4){(float)i0.x, (float)i0.y, (float)i0.z, (float)i0.w} * sv[bj][0]; a1 = (f32x4){(float)i1.x, (float)i1.y, (float)i1.z, (float)i1.w} * sv[bj][1]; }
;                     const f32x4 g0 = a0 * rs[ai][m] + bv[bj][0], g1 = a1 * rs[ai][m] + bv[bj][1];
;                     const f16x8 yy = yv[m][bj];
;                     float z[8];
; #pragma unroll
;                     for (int e = 0; e < 4; ++e) { z[e] = (float)yy[e] * __builtin_amdgcn_rcpf(1.f + __builtin_amdgcn_exp2f(-LOG2E * g0[e])); z[4 + e] = (float)yy[4 + e] * __builtin_amdgcn_rcpf(1.f + __builtin_amdgcn_exp2f(-LOG2E * g1[e])); }
;                     if (br == 2) {
; #pragma unroll
;                         for (int e = 0; e < 8; ++e) z[e] += (float)za[bj][e] + (float)zb[bj][e]; }
;                     u32x4 w; w.x = pk2h(z[0], z[1]); w.y = pk2h(z[2], z[3]); w.z = pk2h(z[4], z[5]); w.w = pk2h(z[6], z[7]);
;                     f16* dst = (br == 2) ? merged : Yb;
;                     gst16(dst + off + bj * HALF, w); } } } }
.Lg3j_31765:
	v_cvt_f32_f16_sdwa v79, v146 dst_sel:DWORD dst_unused:UNUSED_PAD src0_sel:WORD_1
	v_cvt_f32_f16_e32 v78, v146
	v_add_f32_e32 v77, 1.0, v77
	v_rcp_f32_e32 v77, v77
	v_cvt_f32_i32_e32 v80, v80
	v_pk_mul_f32 v[74:75], v[74:75], v[78:79]
	v_cvt_f32_f16_sdwa v79, v148 dst_sel:DWORD dst_unused:UNUSED_PAD src0_sel:WORD_1
	v_cvt_f32_f16_e32 v78, v148
	v_cvt_f32_i32_e32 v81, v81
	v_cvt_f32_f16_sdwa v99, v147 dst_sel:DWORD dst_unused:UNUSED_PAD src0_sel:WORD_1
	v_cvt_f32_f16_e32 v98, v147
	v_pk_mul_f32 v[76:77], v[76:77], v[78:79]
	v_mul_f32_e32 v79, v56, v100
	v_fma_f32 v79, v212, v79, v52
	v_mul_f32_e32 v79, 0xbfb8aa3b, v79
	v_exp_f32_e32 v79, v79
	v_mul_f32_e32 v78, v72, v80
	v_fma_f32 v78, v212, v78, v64
	v_mul_f32_e32 v78, 0xbfb8aa3b, v78
	v_add_f32_e32 v79, 1.0, v79
	v_rcp_f32_e32 v80, v79
	v_mul_f32_e32 v79, v73, v81
	v_mul_f32_e32 v81, v57, v101
	v_fma_f32 v79, v212, v79, v65
	v_fma_f32 v81, v212, v81, v53
	v_mul_f32_e32 v79, 0xbfb8aa3b, v79
	v_mul_f32_e32 v81, 0xbfb8aa3b, v81
	v_exp_f32_e32 v78, v78
	v_exp_f32_e32 v79, v79
	v_exp_f32_e32 v81, v81
	v_cvt_f32_f16_sdwa v95, v149 dst_sel:DWORD dst_unused:UNUSED_PAD src0_sel:WORD_1
	v_add_f32_e32 v78, 1.0, v78
	v_add_f32_e32 v79, 1.0, v79
	v_add_f32_e32 v81, 1.0, v81
	v_rcp_f32_e32 v78, v78
	v_rcp_f32_e32 v79, v79
	v_rcp_f32_e32 v81, v81
	v_cvt_f32_f16_e32 v94, v149
	s_and_b64 vcc, exec, s[36:37]
	v_pk_mul_f32 v[78:79], v[78:79], v[98:99]
	v_pk_mul_f32 v[80:81], v[80:81], v[94:95]
	s_cbranch_vccnz .LBB0_1283
	v_cvt_f32_f16_sdwa v95, v58 dst_sel:DWORD dst_unused:UNUSED_PAD src0_sel:WORD_1
	v_cvt_f32_f16_e32 v94, v58
	s_waitcnt vmcnt(1)
	v_cvt_f32_f16_sdwa v97, v66 dst_sel:DWORD dst_unused:UNUSED_PAD src0_sel:WORD_1
	v_cvt_f32_f16_e32 v96, v66
	v_cvt_f32_f16_sdwa v99, v59 dst_sel:DWORD dst_unused:UNUSED_PAD src0_sel:WORD_1
	v_cvt_f32_f16_e32 v98, v59
	v_cvt_f32_f16_sdwa v101, v67 dst_sel:DWORD dst_unused:UNUSED_PAD src0_sel:WORD_1
	v_cvt_f32_f16_e32 v100, v67
	v_cvt_f32_f16_sdwa v103, v60 dst_sel:DWORD dst_unused:UNUSED_PAD src0_sel:WORD_1
	v_cvt_f32_f16_e32 v102, v60
	v_cvt_f32_f16_sdwa v105, v68 dst_sel:DWORD dst_unused:UNUSED_PAD src0_sel:WORD_1
	v_cvt_f32_f16_e32 v104, v68
	v_cvt_f32_f16_sdwa v109, v61 dst_sel:DWORD dst_unused:UNUSED_PAD src0_sel:WORD_1
	v_cvt_f32_f16_e32 v108, v61
	v_cvt_f32_f16_sdwa v111, v69 dst_sel:DWORD dst_unused:UNUSED_PAD src0_sel:WORD_1
	v_cvt_f32_f16_e32 v110, v69
	v_pk_add_f32 v[94:95], v[96:97], v[94:95]
	v_pk_add_f32 v[96:97], v[100:101], v[98:99]
	v_pk_add_f32 v[98:99], v[104:105], v[102:103]
	v_pk_add_f32 v[100:101], v[110:111], v[108:109]
	v_pk_add_f32 v[74:75], v[74:75], v[94:95]
	v_pk_add_f32 v[78:79], v[78:79], v[96:97]
	v_pk_add_f32 v[76:77], v[76:77], v[98:99]
	v_pk_add_f32 v[80:81], v[80:81], v[100:101]
.LBB0_1283:
	s_mov_b32 s26, 0x10000
	v_cvt_pk_f16_f32 v74, v74, v75
	v_cvt_pk_f16_f32 v75, v78, v79
	v_add_co_u32_e32 v78, vcc, s26, v106
	v_cvt_pk_f16_f32 v76, v76, v77
	v_cvt_pk_f16_f32 v77, v80, v81
	v_addc_co_u32_e32 v79, vcc, 0, v107, vcc
	global_store_dwordx4 v[78:79], v[74:77], off
	v_cvt_f32_i32_e32 v22, v22
	v_cvt_f32_i32_e32 v23, v23
	v_cvt_f32_i32_e32 v74, v24
	v_cvt_f32_i32_e32 v24, v18
	v_cvt_f32_i32_e32 v76, v19
	v_mul_f32_e32 v18, v38, v22
	v_fma_f32 v18, v212, v18, v34
	v_mul_f32_e32 v19, v30, v24
	v_fma_f32 v19, v212, v19, v26
	v_mul_f32_e32 v19, 0xbfb8aa3b, v19
	v_exp_f32_e32 v19, v19
	v_mul_f32_e32 v18, 0xbfb8aa3b, v18
	v_exp_f32_e32 v18, v18
	v_cvt_f32_i32_e32 v75, v25
	v_add_f32_e32 v19, 1.0, v19
	v_rcp_f32_e32 v22, v19
	v_mul_f32_e32 v19, v39, v23
	v_fma_f32 v19, v212, v19, v35
	v_mul_f32_e32 v19, 0xbfb8aa3b, v19
	v_exp_f32_e32 v19, v19
	v_mul_f32_e32 v23, v31, v76
	v_fma_f32 v23, v212, v23, v27
	v_mul_f32_e32 v23, 0xbfb8aa3b, v23
	v_add_f32_e32 v18, 1.0, v18
	v_add_f32_e32 v19, 1.0, v19
	v_exp_f32_e32 v23, v23
	v_rcp_f32_e32 v18, v18
	v_rcp_f32_e32 v19, v19
	s_cmp_lg_u64 s[36:37], 0
	s_cbranch_scc0 .Lg3w_31871
	s_waitcnt vmcnt(7)
	s_branch .Lg3j_31871

; __device__ __forceinline__ unsigned pk2h(float lo, float hi) { f32x2 v = {lo, hi}; f16x2 h = __builtin_convertvector(v, f16x2); return __builtin_bit_cast(unsigned, h); }
;     __device__ __forceinline__ void operator()(const f32x4 (&acc)[2][2][4][2], const Unit& u, int wr, int wc, int fr, int fq) const {
;     ...
;                     f32x4 a0 = acc[ai][bj][m][0], a1 = acc[ai][bj][m][1];
;                     if constexpr (I8) { const i32x4 i0 = __builtin_bit_cast(i32x4, a0), i1 = __builtin_bit_cast(i32x4, a1);
;                         a0 = (f32x4){(float)i0.x, (float)i0.y, (float)i0.z, (float)i0.w} * sv[bj][0]; a1 = (f32x4){(float)i1.x, (float)i1.y, (float)i1.z, (float)i1.w} * sv[bj][1]; }
;                     const f32x4 g0 = a0 * rs[ai][m] + bv[bj][0], g1 = a1 * rs[ai][m] + bv[bj][1];
;                     const f16x8 yy = yv[m][bj];
;                     float z[8];
; #pragma unroll
;                     for (int e = 0; e < 4; ++e) { z[e] = (float)yy[e] * __builtin_amdgcn_rcpf(1.f + __builtin_amdgcn_exp2f(-LOG2E * g0[e])); z[4 + e] = (float)yy[4 + e] * __builtin_amdgcn_rcpf(1.f + __builtin_amdgcn_exp2f(-LOG2E * g1[e])); }
;                     if (br == 2) {
; #pragma unroll
;                         for (int e = 0; e < 8; ++e) z[e] += (float)za[bj][e] + (float)zb[bj][e]; }
;                     u32x4 w; w.x = pk2h(z[0], z[1]); w.y = pk2h(z[2], z[3]); w.z = pk2h(z[4], z[5]); w.w = pk2h(z[6], z[7]);
;                     f16* dst = (br == 2) ? merged : Yb;
;                     gst16(dst + off + bj * HALF, w); } } } }
.Lg3j_31871:
	v_cvt_f32_f16_sdwa v25, v150 dst_sel:DWORD dst_unused:UNUSED_PAD src0_sel:WORD_1
	v_cvt_f32_f16_e32 v24, v150
	v_add_f32_e32 v23, 1.0, v23
	v_rcp_f32_e32 v23, v23
	s_mov_b64 s[46:47], -1
	v_pk_mul_f32 v[18:19], v[18:19], v[24:25]
	v_cvt_f32_f16_sdwa v25, v152 dst_sel:DWORD dst_unused:UNUSED_PAD src0_sel:WORD_1
	v_cvt_f32_f16_e32 v24, v152
	s_and_b64 vcc, exec, s[38:39]
	v_pk_mul_f32 v[22:23], v[22:23], v[24:25]
	v_mul_f32_e32 v24, v40, v74
	v_mul_f32_e32 v25, v41, v75
	v_fma_f32 v24, v212, v24, v36
	v_fma_f32 v25, v212, v25, v37
	v_mul_f32_e32 v24, 0xbfb8aa3b, v24
	v_mul_f32_e32 v25, 0xbfb8aa3b, v25
	v_exp_f32_e32 v24, v24
	v_exp_f32_e32 v25, v25
	v_cvt_f32_f16_sdwa v75, v151 dst_sel:DWORD dst_unused:UNUSED_PAD src0_sel:WORD_1
	v_cvt_f32_f16_e32 v74, v151
	v_add_f32_e32 v24, 1.0, v24
	v_add_f32_e32 v25, 1.0, v25
	v_rcp_f32_e32 v24, v24
	v_rcp_f32_e32 v25, v25
	s_nop 0
	v_pk_mul_f32 v[24:25], v[24:25], v[74:75]
	s_cbranch_vccnz .LBB0_1285
	s_mov_b64 s[46:47], 0
.LBB0_1285:
	v_cvt_f32_i32_e32 v20, v20
	v_cvt_f32_i32_e32 v21, v21
	v_cvt_f32_f16_sdwa v75, v153 dst_sel:DWORD dst_unused:UNUSED_PAD src0_sel:WORD_1
	v_cvt_f32_f16_e32 v74, v153
	v_mul_f32_e32 v20, v32, v20
	v_mul_f32_e32 v21, v33, v21
	v_fma_f32 v20, v212, v20, v28
	v_fma_f32 v21, v212, v21, v29
	v_mul_f32_e32 v20, 0xbfb8aa3b, v20
	v_mul_f32_e32 v21, 0xbfb8aa3b, v21
	v_exp_f32_e32 v20, v20
	v_exp_f32_e32 v21, v21
	s_andn2_b64 vcc, exec, s[46:47]
	v_add_f32_e32 v20, 1.0, v20
	v_add_f32_e32 v21, 1.0, v21
	v_rcp_f32_e32 v20, v20
	v_rcp_f32_e32 v21, v21
	s_nop 0
	v_pk_mul_f32 v[20:21], v[20:21], v[74:75]
	s_cbranch_vccnz .LBB0_1287
	v_cvt_f32_f16_sdwa v75, v42 dst_sel:DWORD dst_unused:UNUSED_PAD src0_sel:WORD_1
	v_cvt_f32_f16_e32 v74, v42
	s_waitcnt vmcnt(1)
	v_cvt_f32_f16_sdwa v77, v46 dst_sel:DWORD dst_unused:UNUSED_PAD src0_sel:WORD_1
	v_cvt_f32_f16_e32 v76, v46
	v_cvt_f32_f16_sdwa v79, v43 dst_sel:DWORD dst_unused:UNUSED_PAD src0_sel:WORD_1
	v_cvt_f32_f16_e32 v78, v43
	v_cvt_f32_f16_sdwa v81, v47 dst_sel:DWORD dst_unused:UNUSED_PAD src0_sel:WORD_1
	v_cvt_f32_f16_e32 v80, v47
	v_cvt_f32_f16_sdwa v91, v44 dst_sel:DWORD dst_unused:UNUSED_PAD src0_sel:WORD_1
	v_cvt_f32_f16_e32 v90, v44
	v_cvt_f32_f16_sdwa v93, v48 dst_sel:DWORD dst_unused:UNUSED_PAD src0_sel:WORD_1
	v_cvt_f32_f16_e32 v92, v48
	v_cvt_f32_f16_sdwa v95, v45 dst_sel:DWORD dst_unused:UNUSED_PAD src0_sel:WORD_1
	v_cvt_f32_f16_e32 v94, v45
	v_cvt_f32_f16_sdwa v97, v49 dst_sel:DWORD dst_unused:UNUSED_PAD src0_sel:WORD_1
	v_cvt_f32_f16_e32 v96, v49
	v_pk_add_f32 v[74:75], v[76:77], v[74:75]
	v_pk_add_f32 v[76:77], v[80:81], v[78:79]
	v_pk_add_f32 v[78:79], v[92:93], v[90:91]
	v_pk_add_f32 v[80:81], v[96:97], v[94:95]
	v_pk_add_f32 v[18:19], v[18:19], v[74:75]
	v_pk_add_f32 v[24:25], v[24:25], v[76:77]
	v_pk_add_f32 v[22:23], v[22:23], v[78:79]
	v_pk_add_f32 v[20:21], v[20:21], v[80:81]

;     __device__ __forceinline__ void operator()(const f32x4 (&acc)[2][2][4][2], const Unit& u, int wr, int wc, int fr, int fq) const {
;     ...
;                     f32x4 a0 = acc[ai][bj][m][0], a1 = acc[ai][bj][m][1];
;                     if constexpr (I8) { const i32x4 i0 = __builtin_bit_cast(i32x4, a0), i1 = __builtin_bit_cast(i32x4, a1);
;                         a0 = (f32x4){(float)i0.x, (float)i0.y, (float)i0.z, (float)i0.w} * sv[bj][0]; a1 = (f32x4){(float)i1.x, (float)i1.y, (float)i1.z, (float)i1.w} * sv[bj][1]; }
;                     const f32x4 g0 = a0 * rs[ai][m] + bv[bj][0], g1 = a1 * rs[ai][m] + bv[bj][1];
;                     const f16x8 yy = yv[m][bj];
;                     float z[8];
; #pragma unroll
;                     for (int e = 0; e < 4; ++e) { z[e] = (float)yy[e] * __builtin_amdgcn_rcpf(1.f + __builtin_amdgcn_exp2f(-LOG2E * g0[e])); z[4 + e] = (float)yy[4 + e] * __builtin_amdgcn_rcpf(1.f + __builtin_amdgcn_exp2f(-LOG2E * g1[e])); }
.LBB0_1289:
	v_cvt_f32_i32_e32 v14, v14
	v_cvt_f32_i32_e32 v15, v15
	v_cvt_f32_i32_e32 v18, v10
	v_cvt_f32_i32_e32 v19, v12
	v_mul_f32_e32 v10, v70, v14
	v_mul_f32_e32 v12, v71, v15
	v_fma_f32 v10, v213, v10, v62
	v_cvt_f32_i32_e32 v14, v11
	v_fma_f32 v12, v213, v12, v63
	v_mul_f32_e32 v10, 0xbfb8aa3b, v10
	v_mul_f32_e32 v12, 0xbfb8aa3b, v12
	v_exp_f32_e32 v10, v10
	v_exp_f32_e32 v12, v12
	v_mul_f32_e32 v11, v54, v18
	v_fma_f32 v11, v213, v11, v50
	v_mul_f32_e32 v14, v55, v14
	v_mul_f32_e32 v11, 0xbfb8aa3b, v11
	v_fma_f32 v14, v213, v14, v51
	v_add_f32_e32 v10, 1.0, v10
	v_exp_f32_e32 v15, v11
	v_add_f32_e32 v11, 1.0, v12
	v_mul_f32_e32 v14, 0xbfb8aa3b, v14
	v_cvt_f32_i32_e32 v16, v16
	v_cvt_f32_i32_e32 v17, v17
	v_cvt_f32_i32_e32 v20, v13
	v_rcp_f32_e32 v10, v10
	v_rcp_f32_e32 v11, v11
	s_cmp_lg_u64 s[36:37], 0
	s_cbranch_scc0 .Lg3w_31995
	s_waitcnt vmcnt(7)
	s_branch .Lg3j_31995

; __device__ __forceinline__ unsigned pk2h(float lo, float hi) { f32x2 v = {lo, hi}; f16x2 h = __builtin_convertvector(v, f16x2); return __builtin_bit_cast(unsigned, h); }
;     __device__ __forceinline__ void operator()(const f32x4 (&acc)[2][2][4][2], const Unit& u, int wr, int wc, int fr, int fq) const {
;     ...
;                     f32x4 a0 = acc[ai][bj][m][0], a1 = acc[ai][bj][m][1];
;                     if constexpr (I8) { const i32x4 i0 = __builtin_bit_cast(i32x4, a0), i1 = __builtin_bit_cast(i32x4, a1);
;                         a0 = (f32x4){(float)i0.x, (float)i0.y, (float)i0.z, (float)i0.w} * sv[bj][0]; a1 = (f32x4){(float)i1.x, (float)i1.y, (float)i1.z, (float)i1.w} * sv[bj][1]; }
;                     const f32x4 g0 = a0 * rs[ai][m] + bv[bj][0], g1 = a1 * rs[ai][m] + bv[bj][1];
;                     const f16x8 yy = yv[m][bj];
;                     float z[8];
; #pragma unroll
;                     for (int e = 0; e < 4; ++e) { z[e] = (float)yy[e] * __builtin_amdgcn_rcpf(1.f + __builtin_amdgcn_exp2f(-LOG2E * g0[e])); z[4 + e] = (float)yy[4 + e] * __builtin_amdgcn_rcpf(1.f + __builtin_amdgcn_exp2f(-LOG2E * g1[e])); }
;                     if (br == 2) {
; #pragma unroll
;                         for (int e = 0; e < 8; ++e) z[e] += (float)za[bj][e] + (float)zb[bj][e]; }
;                     u32x4 w; w.x = pk2h(z[0], z[1]); w.y = pk2h(z[2], z[3]); w.z = pk2h(z[4], z[5]); w.w = pk2h(z[6], z[7]);
;                     f16* dst = (br == 2) ? merged : Yb;
;                     gst16(dst + off + bj * HALF, w); } } } }
.Lg3j_31995:
	v_cvt_f32_f16_sdwa v13, v154 dst_sel:DWORD dst_unused:UNUSED_PAD src0_sel:WORD_1
	v_cvt_f32_f16_e32 v12, v154
	v_exp_f32_e32 v18, v14
	v_mul_f32_e32 v17, v73, v17
	v_fmac_f32_e32 v65, v213, v17
	v_pk_mul_f32 v[10:11], v[10:11], v[12:13]
	v_add_f32_e32 v12, 1.0, v18
	v_mul_f32_e32 v13, v72, v16
	v_mul_f32_e32 v18, v56, v19
	v_mul_f32_e32 v19, v57, v20
	v_fma_f32 v13, v213, v13, v64
	v_fma_f32 v18, v213, v18, v52
	v_fmac_f32_e32 v53, v213, v19
	v_mul_f32_e32 v13, 0xbfb8aa3b, v13
	v_mul_f32_e32 v18, 0xbfb8aa3b, v18
	v_mul_f32_e32 v17, 0xbfb8aa3b, v65
	v_mul_f32_e32 v19, 0xbfb8aa3b, v53
	v_exp_f32_e32 v16, v13
	v_exp_f32_e32 v18, v18
	v_exp_f32_e32 v17, v17
	v_exp_f32_e32 v19, v19
	v_add_f32_e32 v14, 1.0, v15
	v_add_f32_e32 v16, 1.0, v16
	v_add_f32_e32 v18, 1.0, v18
	v_add_f32_e32 v17, 1.0, v17
	v_add_f32_e32 v19, 1.0, v19
	v_rcp_f32_e32 v14, v14
	v_rcp_f32_e32 v15, v12
	v_cvt_f32_f16_sdwa v13, v156 dst_sel:DWORD dst_unused:UNUSED_PAD src0_sel:WORD_1
	v_cvt_f32_f16_e32 v12, v156
	v_rcp_f32_e32 v16, v16
	v_rcp_f32_e32 v18, v18
	v_rcp_f32_e32 v17, v17
	v_cvt_f32_f16_sdwa v21, v155 dst_sel:DWORD dst_unused:UNUSED_PAD src0_sel:WORD_1
	v_cvt_f32_f16_e32 v20, v155
	v_rcp_f32_e32 v19, v19
	v_cvt_f32_f16_sdwa v23, v157 dst_sel:DWORD dst_unused:UNUSED_PAD src0_sel:WORD_1
	v_cvt_f32_f16_e32 v22, v157
	v_pk_mul_f32 v[12:13], v[14:15], v[12:13]
	v_pk_mul_f32 v[14:15], v[16:17], v[20:21]
	s_and_b64 vcc, exec, s[36:37]
	v_pk_mul_f32 v[16:17], v[18:19], v[22:23]
	s_cbranch_vccnz .LBB0_1291
	v_cvt_f32_f16_sdwa v19, v58 dst_sel:DWORD dst_unused:UNUSED_PAD src0_sel:WORD_1
	v_cvt_f32_f16_e32 v18, v58
	s_waitcnt vmcnt(1)
	v_cvt_f32_f16_sdwa v21, v66 dst_sel:DWORD dst_unused:UNUSED_PAD src0_sel:WORD_1
	v_cvt_f32_f16_e32 v20, v66
	v_cvt_f32_f16_sdwa v23, v59 dst_sel:DWORD dst_unused:UNUSED_PAD src0_sel:WORD_1
	v_cvt_f32_f16_e32 v22, v59
	v_cvt_f32_f16_sdwa v25, v67 dst_sel:DWORD dst_unused:UNUSED_PAD src0_sel:WORD_1
	v_cvt_f32_f16_e32 v24, v67
	v_cvt_f32_f16_sdwa v51, v60 dst_sel:DWORD dst_unused:UNUSED_PAD src0_sel:WORD_1
	v_cvt_f32_f16_e32 v50, v60
	v_cvt_f32_f16_sdwa v53, v68 dst_sel:DWORD dst_unused:UNUSED_PAD src0_sel:WORD_1
	v_cvt_f32_f16_e32 v52, v68
	v_cvt_f32_f16_sdwa v55, v61 dst_sel:DWORD dst_unused:UNUSED_PAD src0_sel:WORD_1
	v_cvt_f32_f16_e32 v54, v61
	v_cvt_f32_f16_sdwa v57, v69 dst_sel:DWORD dst_unused:UNUSED_PAD src0_sel:WORD_1
	v_cvt_f32_f16_e32 v56, v69
	v_pk_add_f32 v[18:19], v[20:21], v[18:19]
	v_pk_add_f32 v[20:21], v[24:25], v[22:23]
	v_pk_add_f32 v[22:23], v[52:53], v[50:51]
	v_pk_add_f32 v[24:25], v[56:57], v[54:55]
	v_pk_add_f32 v[10:11], v[10:11], v[18:19]
	v_pk_add_f32 v[14:15], v[14:15], v[20:21]
	v_pk_add_f32 v[12:13], v[12:13], v[22:23]
	v_pk_add_f32 v[16:17], v[16:17], v[24:25]
.LBB0_1291:
	v_cvt_f32_i32_e32 v6, v6
	v_cvt_f32_i32_e32 v7, v7
	s_mov_b32 s26, 0x18000
	v_cvt_pk_f16_f32 v10, v10, v11
	v_cvt_pk_f16_f32 v11, v14, v15
	v_add_co_u32_e32 v14, vcc, s26, v106
	v_cvt_pk_f16_f32 v12, v12, v13
	v_cvt_pk_f16_f32 v13, v16, v17
	v_addc_co_u32_e32 v15, vcc, 0, v107, vcc
	global_store_dwordx4 v[14:15], v[10:13], off
	v_cvt_f32_i32_e32 v8, v8
	v_cvt_f32_i32_e32 v9, v9
	v_cvt_f32_i32_e32 v10, v2
	v_mul_f32_e32 v2, v38, v6
	v_cvt_f32_i32_e32 v11, v4
	v_mul_f32_e32 v4, v39, v7
	v_fma_f32 v2, v213, v2, v34
	v_cvt_f32_i32_e32 v6, v3
	v_fma_f32 v4, v213, v4, v35
	v_mul_f32_e32 v2, 0xbfb8aa3b, v2
	v_mul_f32_e32 v4, 0xbfb8aa3b, v4
	v_exp_f32_e32 v2, v2
	v_exp_f32_e32 v4, v4
	v_mul_f32_e32 v3, v30, v10
	v_fma_f32 v3, v213, v3, v26
	v_mul_f32_e32 v6, v31, v6
	v_mul_f32_e32 v3, 0xbfb8aa3b, v3
	v_fma_f32 v6, v213, v6, v27
	v_add_f32_e32 v2, 1.0, v2
	v_exp_f32_e32 v7, v3
	v_add_f32_e32 v3, 1.0, v4
	v_mul_f32_e32 v6, 0xbfb8aa3b, v6
	v_cvt_f32_i32_e32 v12, v5
	v_rcp_f32_e32 v2, v2
	v_rcp_f32_e32 v3, v3
	s_cmp_lg_u64 s[36:37], 0
	s_cbranch_scc0 .Lg3w_32101
	s_waitcnt vmcnt(7)
	s_branch .Lg3j_32101

;     __device__ __forceinline__ void operator()(const f32x4 (&acc)[2][2][4][2], const Unit& u, int wr, int wc, int fr, int fq) const {
;     ...
;                     f32x4 a0 = acc[ai][bj][m][0], a1 = acc[ai][bj][m][1];
;                     if constexpr (I8) { const i32x4 i0 = __builtin_bit_cast(i32x4, a0), i1 = __builtin_bit_cast(i32x4, a1);
;                         a0 = (f32x4){(float)i0.x, (float)i0.y, (float)i0.z, (float)i0.w} * sv[bj][0]; a1 = (f32x4){(float)i1.x, (float)i1.y, (float)i1.z, (float)i1.w} * sv[bj][1]; }
;                     const f32x4 g0 = a0 * rs[ai][m] + bv[bj][0], g1 = a1 * rs[ai][m] + bv[bj][1];
;                     const f16x8 yy = yv[m][bj];
;                     float z[8];
; #pragma unroll
;                     for (int e = 0; e < 4; ++e) { z[e] = (float)yy[e] * __builtin_amdgcn_rcpf(1.f + __builtin_amdgcn_exp2f(-LOG2E * g0[e])); z[4 + e] = (float)yy[4 + e] * __builtin_amdgcn_rcpf(1.f + __builtin_amdgcn_exp2f(-LOG2E * g1[e])); }
;                     if (br == 2) {
; #pragma unroll
;                         for (int e = 0; e < 8; ++e) z[e] += (float)za[bj][e] + (float)zb[bj][e]; }
.Lg3j_32101:
	v_cvt_f32_f16_sdwa v5, v158 dst_sel:DWORD dst_unused:UNUSED_PAD src0_sel:WORD_1
	v_cvt_f32_f16_e32 v4, v158
	v_exp_f32_e32 v10, v6
	v_mul_f32_e32 v9, v41, v9
	v_fmac_f32_e32 v37, v213, v9
	v_pk_mul_f32 v[2:3], v[2:3], v[4:5]
	v_add_f32_e32 v4, 1.0, v10
	v_mul_f32_e32 v5, v40, v8
	v_mul_f32_e32 v10, v32, v11
	v_mul_f32_e32 v11, v33, v12
	v_fma_f32 v5, v213, v5, v36
	v_fma_f32 v10, v213, v10, v28
	v_fmac_f32_e32 v29, v213, v11
	v_mul_f32_e32 v5, 0xbfb8aa3b, v5
	v_mul_f32_e32 v10, 0xbfb8aa3b, v10
	v_mul_f32_e32 v9, 0xbfb8aa3b, v37
	v_mul_f32_e32 v11, 0xbfb8aa3b, v29
	v_exp_f32_e32 v8, v5
	v_exp_f32_e32 v10, v10
	v_exp_f32_e32 v9, v9
	v_exp_f32_e32 v11, v11
	v_add_f32_e32 v6, 1.0, v7
	v_add_f32_e32 v8, 1.0, v8
	v_add_f32_e32 v10, 1.0, v10
	v_add_f32_e32 v9, 1.0, v9
	v_add_f32_e32 v11, 1.0, v11
	v_rcp_f32_e32 v6, v6
	v_rcp_f32_e32 v7, v4
	v_cvt_f32_f16_sdwa v5, v160 dst_sel:DWORD dst_unused:UNUSED_PAD src0_sel:WORD_1
	v_cvt_f32_f16_e32 v4, v160
	v_rcp_f32_e32 v8, v8
	v_rcp_f32_e32 v10, v10
	v_rcp_f32_e32 v9, v9
	v_cvt_f32_f16_sdwa v13, v159 dst_sel:DWORD dst_unused:UNUSED_PAD src0_sel:WORD_1
	v_cvt_f32_f16_e32 v12, v159
	v_rcp_f32_e32 v11, v11
	v_cvt_f32_f16_sdwa v15, v161 dst_sel:DWORD dst_unused:UNUSED_PAD src0_sel:WORD_1
	v_cvt_f32_f16_e32 v14, v161
	v_pk_mul_f32 v[4:5], v[6:7], v[4:5]
	v_pk_mul_f32 v[6:7], v[8:9], v[12:13]
	s_and_b64 vcc, exec, s[36:37]
	v_pk_mul_f32 v[8:9], v[10:11], v[14:15]
	s_cbranch_vccnz .LBB0_1293
	v_cvt_f32_f16_sdwa v11, v42 dst_sel:DWORD dst_unused:UNUSED_PAD src0_sel:WORD_1
	v_cvt_f32_f16_e32 v10, v42
	s_waitcnt vmcnt(1)
	v_cvt_f32_f16_sdwa v13, v46 dst_sel:DWORD dst_unused:UNUSED_PAD src0_sel:WORD_1
	v_cvt_f32_f16_e32 v12, v46
	v_cvt_f32_f16_sdwa v15, v43 dst_sel:DWORD dst_unused:UNUSED_PAD src0_sel:WORD_1
	v_cvt_f32_f16_e32 v14, v43
	v_cvt_f32_f16_sdwa v17, v47 dst_sel:DWORD dst_unused:UNUSED_PAD src0_sel:WORD_1
	v_cvt_f32_f16_e32 v16, v47
	v_cvt_f32_f16_sdwa v19, v44 dst_sel:DWORD dst_unused:UNUSED_PAD src0_sel:WORD_1
	v_cvt_f32_f16_e32 v18, v44
	v_cvt_f32_f16_sdwa v21, v48 dst_sel:DWORD dst_unused:UNUSED_PAD src0_sel:WORD_1
	v_cvt_f32_f16_e32 v20, v48
	v_cvt_f32_f16_sdwa v23, v45 dst_sel:DWORD dst_unused:UNUSED_PAD src0_sel:WORD_1
	v_cvt_f32_f16_e32 v22, v45
	v_cvt_f32_f16_sdwa v25, v49 dst_sel:DWORD dst_unused:UNUSED_PAD src0_sel:WORD_1
	v_cvt_f32_f16_e32 v24, v49
	v_pk_add_f32 v[10:11], v[12:13], v[10:11]
	v_pk_add_f32 v[12:13], v[16:17], v[14:15]
	v_pk_add_f32 v[14:15], v[20:21], v[18:19]
	v_pk_add_f32 v[16:17], v[24:25], v[22:23]
	v_pk_add_f32 v[2:3], v[2:3], v[10:11]
	v_pk_add_f32 v[6:7], v[6:7], v[12:13]
	v_pk_add_f32 v[4:5], v[4:5], v[14:15]
	v_pk_add_f32 v[8:9], v[8:9], v[16:17]
